# loop-edge edit: hipcc's per-lane materialisation of the wave-uniform !has_next mask (v_cndmask + v_cmp_ne) replaced by one s_andn2_b64 with exec at 4 grouped-GEMM loop sites
# baseline (speedup 1.0000x reference)
.LBB0_1540:
	s_nop 0
	s_andn2_b64 s[6:7], exec, s[8:9]
	s_andn2_b64 vcc, exec, s[8:9]
	v_mov_b32_e32 v148, v150
	v_mov_b32_e32 v146, v152
	v_mov_b32_e32 v170, v154
	v_mov_b32_e32 v169, v142
	s_cbranch_vccnz .LBB0_1542
	s_ashr_i32 s73, s72, 31
	s_lshl_b64 s[76:77], s[72:73], 10
	s_add_u32 s76, s4, s76
	s_addc_u32 s77, s5, s77
	global_load_dword v246, v1, s[76:77]
	global_load_dword v247, v160, s[76:77]
	global_load_dword v248, v160, s[76:77] offset:512
	global_load_dword v249, v1, s[76:77] offset:512

.LBB0_1623:
	s_ashr_i32 s41, s40, 31
	s_lshl_b64 s[8:9], s[40:41], 18
	s_add_u32 s44, s33, s8
	ds_read_b128 v[10:13], v162
	ds_read_b128 v[14:17], v162 offset:1024
	ds_read_b128 v[26:29], v162 offset:2048
	ds_read_b128 v[30:33], v162 offset:3072
	ds_read_b128 v[172:175], v163
	ds_read_b128 v[176:179], v163 offset:1024
	ds_read_b128 v[180:183], v163 offset:2048
	ds_read_b128 v[184:187], v163 offset:3072
	s_addc_u32 s45, s37, s9
	s_and_b64 s[8:9], s[6:7], exec
	s_cselect_b32 s75, s45, s69
	s_cselect_b32 s74, s44, s68
	s_ashr_i32 s43, s42, 31
	s_ashr_i32 s39, s38, 31
	s_lshl_b64 s[8:9], s[42:43], 20
	s_lshl_b64 s[46:47], s[38:39], 18
	s_add_u32 s8, s54, s8
	s_addc_u32 s9, s55, s9
	s_add_u32 s46, s8, s46
	s_addc_u32 s47, s9, s47
	s_and_b64 s[8:9], s[6:7], exec
	s_cselect_b32 s9, s47, s73
	s_cselect_b32 s8, s46, s72
	ds_read_b128 v[18:21], v161
	ds_read_b128 v[22:25], v161 offset:1024
	ds_read_b128 v[34:37], v161 offset:2048
	ds_read_b128 v[38:41], v161 offset:3072
	ds_read_b128 v[42:45], v161 offset:4096
	ds_read_b128 v[46:49], v161 offset:5120
	ds_read_b128 v[50:53], v161 offset:6144
	ds_read_b128 v[54:57], v161 offset:7168
	s_waitcnt vmcnt(16)
	s_waitcnt lgkmcnt(0)
	s_barrier
	s_setprio 1
	s_waitcnt lgkmcnt(0)
	v_mfma_f32_16x16x128_f8f6f4 v[134:137], v[10:17], v[18:25], 0
	v_mfma_f32_16x16x128_f8f6f4 v[130:133], v[26:33], v[18:25], 0
	v_mfma_f32_16x16x128_f8f6f4 v[118:121], v[10:17], v[34:41], 0
	v_mfma_f32_16x16x128_f8f6f4 v[114:117], v[26:33], v[34:41], 0
	v_mfma_f32_16x16x128_f8f6f4 v[102:105], v[10:17], v[42:49], 0
	v_mfma_f32_16x16x128_f8f6f4 v[98:101], v[26:33], v[42:49], 0
	v_mfma_f32_16x16x128_f8f6f4 v[78:81], v[10:17], v[50:57], 0
	v_mfma_f32_16x16x128_f8f6f4 v[74:77], v[26:33], v[50:57], 0
	s_setprio 0
	s_setprio 1
	v_mfma_f32_16x16x128_f8f6f4 v[126:129], v[172:179], v[18:25], 0
	v_mfma_f32_16x16x128_f8f6f4 v[122:125], v[180:187], v[18:25], 0
	v_mfma_f32_16x16x128_f8f6f4 v[110:113], v[172:179], v[34:41], 0
	v_mfma_f32_16x16x128_f8f6f4 v[106:109], v[180:187], v[34:41], 0
	v_mfma_f32_16x16x128_f8f6f4 v[94:97], v[172:179], v[42:49], 0
	v_mfma_f32_16x16x128_f8f6f4 v[90:93], v[180:187], v[42:49], 0
	v_mfma_f32_16x16x128_f8f6f4 v[62:65], v[172:179], v[50:57], 0
	v_mfma_f32_16x16x128_f8f6f4 v[58:61], v[180:187], v[50:57], 0
	s_setprio 0
	s_barrier
	s_add_i32 s80, s66, s58
	v_lshl_add_u64 v[150:151], s[72:73], 0, v[140:141]
	s_add_i32 s76, s80, 0x2000
	v_lshl_add_u64 v[18:19], v[150:151], 0, s[22:23]
	s_mov_b32 m0, s80
	v_lshl_add_u64 v[152:153], s[72:73], 0, v[144:145]
	s_add_u32 s78, s72, 0x8100
	ds_read_b128 v[42:45], v161 offset:16384
	ds_read_b128 v[46:49], v161 offset:17408
	ds_read_b128 v[188:191], v161 offset:18432
	ds_read_b128 v[192:195], v161 offset:19456
	ds_read_b128 v[204:207], v161 offset:20480
	ds_read_b128 v[208:211], v161 offset:21504
	ds_read_b128 v[212:215], v161 offset:22528
	ds_read_b128 v[216:219], v161 offset:23552
	global_load_lds_dwordx4 v[18:19], off
	v_lshl_add_u64 v[18:19], v[152:153], 0, s[22:23]
	s_mov_b32 m0, s76
	s_addc_u32 s79, s73, 0
	s_add_i32 s77, s67, s58
	global_load_lds_dwordx4 v[18:19], off
	v_lshl_add_u64 v[18:19], s[78:79], 0, v[140:141]
	s_mov_b32 m0, s77
	v_lshl_add_u64 v[154:155], s[68:69], 0, v[138:139]
	global_load_lds_dwordx4 v[18:19], off
	v_lshl_add_u64 v[18:19], s[78:79], 0, v[144:145]
	s_add_i32 s78, s77, 0x2000
	s_mov_b32 m0, s78
	v_lshl_add_u64 v[156:157], s[68:69], 0, v[142:143]
	global_load_lds_dwordx4 v[18:19], off
	v_lshl_add_u64 v[18:19], v[154:155], 0, s[22:23]
	s_mov_b32 m0, s49
	s_nop 0
	global_load_lds_dwordx4 v[18:19], off
	v_lshl_add_u64 v[18:19], v[156:157], 0, s[22:23]
	s_mov_b32 m0, s51
	s_nop 0
	global_load_lds_dwordx4 v[18:19], off
	s_waitcnt vmcnt(16)
	s_waitcnt lgkmcnt(0)
	s_barrier
	s_setprio 1
	s_waitcnt lgkmcnt(0)
	v_mfma_f32_16x16x128_f8f6f4 v[86:89], v[10:17], v[42:49], 0
	v_mfma_f32_16x16x128_f8f6f4 v[82:85], v[26:33], v[42:49], 0
	v_mfma_f32_16x16x128_f8f6f4 v[54:57], v[10:17], v[188:195], 0
	v_mfma_f32_16x16x128_f8f6f4 v[50:53], v[26:33], v[188:195], 0
	v_mfma_f32_16x16x128_f8f6f4 v[38:41], v[10:17], v[204:211], 0
	v_mfma_f32_16x16x128_f8f6f4 v[34:37], v[26:33], v[204:211], 0
	v_mfma_f32_16x16x128_f8f6f4 v[22:25], v[10:17], v[212:219], 0
	v_mfma_f32_16x16x128_f8f6f4 v[18:21], v[26:33], v[212:219], 0
	s_setprio 0
	s_setprio 1
	v_mfma_f32_16x16x128_f8f6f4 v[70:73], v[172:179], v[42:49], 0
	v_mfma_f32_16x16x128_f8f6f4 v[66:69], v[180:187], v[42:49], 0
	v_mfma_f32_16x16x128_f8f6f4 v[46:49], v[172:179], v[188:195], 0
	v_mfma_f32_16x16x128_f8f6f4 v[42:45], v[180:187], v[188:195], 0
	v_mfma_f32_16x16x128_f8f6f4 v[30:33], v[172:179], v[204:211], 0
	v_mfma_f32_16x16x128_f8f6f4 v[26:29], v[180:187], v[204:211], 0
	v_mfma_f32_16x16x128_f8f6f4 v[14:17], v[172:179], v[212:219], 0
	v_mfma_f32_16x16x128_f8f6f4 v[10:13], v[180:187], v[212:219], 0
	s_setprio 0
	s_barrier
	s_add_i32 s79, 0, 0x18000
	s_add_i32 s41, 0, 0x1c000
	v_add_u32_e32 v158, s79, v160
	v_add_u32_e32 v159, s41, v160
	ds_read_b128 v[172:175], v158
	ds_read_b128 v[176:179], v158 offset:1024
	ds_read_b128 v[180:183], v158 offset:2048
	ds_read_b128 v[184:187], v158 offset:3072
	ds_read_b128 v[188:191], v159
	ds_read_b128 v[192:195], v159 offset:1024
	ds_read_b128 v[204:207], v159 offset:2048
	ds_read_b128 v[208:211], v159 offset:3072
	s_add_u32 s82, s68, 0x20100
	s_addc_u32 s83, s69, 0
	s_mov_b32 m0, s59
	v_lshl_add_u64 v[196:197], s[82:83], 0, v[138:139]
	ds_read_b128 v[212:215], v161 offset:32768
	ds_read_b128 v[216:219], v161 offset:33792
	ds_read_b128 v[220:223], v161 offset:34816
	ds_read_b128 v[224:227], v161 offset:35840
	ds_read_b128 v[228:231], v161 offset:36864
	ds_read_b128 v[232:235], v161 offset:37888
	ds_read_b128 v[236:239], v161 offset:38912
	ds_read_b128 v[240:243], v161 offset:39936
	global_load_lds_dwordx4 v[196:197], off
	v_lshl_add_u64 v[196:197], s[82:83], 0, v[142:143]
	s_mov_b32 m0, s60
	s_nop 0
	global_load_lds_dwordx4 v[196:197], off
	s_waitcnt vmcnt(16)
	s_waitcnt lgkmcnt(0)
	s_barrier
	s_setprio 1
	s_waitcnt lgkmcnt(0)
	v_mfma_f32_16x16x128_f8f6f4 v[134:137], v[172:179], v[212:219], v[134:137]
	v_mfma_f32_16x16x128_f8f6f4 v[130:133], v[180:187], v[212:219], v[130:133]
	v_mfma_f32_16x16x128_f8f6f4 v[118:121], v[172:179], v[220:227], v[118:121]
	v_mfma_f32_16x16x128_f8f6f4 v[114:117], v[180:187], v[220:227], v[114:117]
	v_mfma_f32_16x16x128_f8f6f4 v[102:105], v[172:179], v[228:235], v[102:105]
	v_mfma_f32_16x16x128_f8f6f4 v[98:101], v[180:187], v[228:235], v[98:101]
	v_mfma_f32_16x16x128_f8f6f4 v[78:81], v[172:179], v[236:243], v[78:81]
	v_mfma_f32_16x16x128_f8f6f4 v[74:77], v[180:187], v[236:243], v[74:77]
	s_setprio 0
	s_setprio 1
	v_mfma_f32_16x16x128_f8f6f4 v[126:129], v[188:195], v[212:219], v[126:129]
	v_mfma_f32_16x16x128_f8f6f4 v[122:125], v[204:211], v[212:219], v[122:125]
	v_mfma_f32_16x16x128_f8f6f4 v[110:113], v[188:195], v[220:227], v[110:113]
	v_mfma_f32_16x16x128_f8f6f4 v[106:109], v[204:211], v[220:227], v[106:109]
	v_mfma_f32_16x16x128_f8f6f4 v[94:97], v[188:195], v[228:235], v[94:97]
	v_mfma_f32_16x16x128_f8f6f4 v[90:93], v[204:211], v[228:235], v[90:93]
	v_mfma_f32_16x16x128_f8f6f4 v[62:65], v[188:195], v[236:243], v[62:65]
	v_mfma_f32_16x16x128_f8f6f4 v[58:61], v[204:211], v[236:243], v[58:61]
	s_setprio 0
	s_barrier
	s_add_i32 s79, s79, s58
	s_add_i32 s39, s79, 0x2000
	v_lshl_add_u64 v[196:197], v[150:151], 0, s[24:25]
	s_mov_b32 m0, s79
	s_add_u32 s82, s72, 0x8180
	ds_read_b128 v[212:215], v161 offset:49152
	ds_read_b128 v[216:219], v161 offset:50176
	ds_read_b128 v[220:223], v161 offset:51200
	ds_read_b128 v[224:227], v161 offset:52224
	ds_read_b128 v[228:231], v161 offset:53248
	ds_read_b128 v[232:235], v161 offset:54272
	ds_read_b128 v[236:239], v161 offset:55296
	ds_read_b128 v[240:243], v161 offset:56320
	global_load_lds_dwordx4 v[196:197], off
	v_lshl_add_u64 v[196:197], v[152:153], 0, s[24:25]
	s_mov_b32 m0, s39
	s_addc_u32 s83, s73, 0
	s_add_i32 s41, s41, s58
	global_load_lds_dwordx4 v[196:197], off
	v_lshl_add_u64 v[196:197], s[82:83], 0, v[140:141]
	s_mov_b32 m0, s41
	s_add_i32 s71, s41, 0x2000
	global_load_lds_dwordx4 v[196:197], off
	v_lshl_add_u64 v[196:197], s[82:83], 0, v[144:145]
	s_mov_b32 m0, s71
	s_nop 0
	global_load_lds_dwordx4 v[196:197], off
	v_lshl_add_u64 v[196:197], v[154:155], 0, s[24:25]
	s_mov_b32 m0, s61
	s_nop 0
	global_load_lds_dwordx4 v[196:197], off
	v_lshl_add_u64 v[196:197], v[156:157], 0, s[24:25]
	s_mov_b32 m0, s62
	s_nop 0
	global_load_lds_dwordx4 v[196:197], off
	s_waitcnt vmcnt(8)
	s_waitcnt lgkmcnt(0)
	s_barrier
	s_setprio 1
	s_waitcnt lgkmcnt(0)
	v_mfma_f32_16x16x128_f8f6f4 v[86:89], v[172:179], v[212:219], v[86:89]
	v_mfma_f32_16x16x128_f8f6f4 v[82:85], v[180:187], v[212:219], v[82:85]
	v_mfma_f32_16x16x128_f8f6f4 v[54:57], v[172:179], v[220:227], v[54:57]
	v_mfma_f32_16x16x128_f8f6f4 v[50:53], v[180:187], v[220:227], v[50:53]
	v_mfma_f32_16x16x128_f8f6f4 v[38:41], v[172:179], v[228:235], v[38:41]
	v_mfma_f32_16x16x128_f8f6f4 v[34:37], v[180:187], v[228:235], v[34:37]
	v_mfma_f32_16x16x128_f8f6f4 v[22:25], v[172:179], v[236:243], v[22:25]
	v_mfma_f32_16x16x128_f8f6f4 v[18:21], v[180:187], v[236:243], v[18:21]
	s_setprio 0
	s_setprio 1
	v_mfma_f32_16x16x128_f8f6f4 v[70:73], v[188:195], v[212:219], v[70:73]
	v_mfma_f32_16x16x128_f8f6f4 v[66:69], v[204:211], v[212:219], v[66:69]
	v_mfma_f32_16x16x128_f8f6f4 v[46:49], v[188:195], v[220:227], v[46:49]
	v_mfma_f32_16x16x128_f8f6f4 v[42:45], v[204:211], v[220:227], v[42:45]
	v_mfma_f32_16x16x128_f8f6f4 v[30:33], v[188:195], v[228:235], v[30:33]
	v_mfma_f32_16x16x128_f8f6f4 v[26:29], v[204:211], v[228:235], v[26:29]
	v_mfma_f32_16x16x128_f8f6f4 v[14:17], v[188:195], v[236:243], v[14:17]
	v_mfma_f32_16x16x128_f8f6f4 v[10:13], v[204:211], v[236:243], v[10:13]
	s_setprio 0
	s_barrier
	ds_read_b128 v[172:175], v162
	ds_read_b128 v[176:179], v162 offset:1024
	ds_read_b128 v[180:183], v162 offset:2048
	ds_read_b128 v[184:187], v162 offset:3072
	ds_read_b128 v[188:191], v163
	ds_read_b128 v[192:195], v163 offset:1024
	ds_read_b128 v[204:207], v163 offset:2048
	ds_read_b128 v[208:211], v163 offset:3072
	s_add_u32 s82, s68, 0x20180
	s_addc_u32 s83, s69, 0
	s_mov_b32 m0, s63
	v_lshl_add_u64 v[196:197], s[82:83], 0, v[138:139]
	ds_read_b128 v[212:215], v161
	ds_read_b128 v[216:219], v161 offset:1024
	ds_read_b128 v[220:223], v161 offset:2048
	ds_read_b128 v[224:227], v161 offset:3072
	ds_read_b128 v[228:231], v161 offset:4096
	ds_read_b128 v[232:235], v161 offset:5120
	ds_read_b128 v[236:239], v161 offset:6144
	ds_read_b128 v[240:243], v161 offset:7168
	global_load_lds_dwordx4 v[196:197], off
	v_lshl_add_u64 v[196:197], s[82:83], 0, v[142:143]
	s_mov_b32 m0, s64
	s_nop 0
	global_load_lds_dwordx4 v[196:197], off
	s_waitcnt vmcnt(8)
	s_waitcnt lgkmcnt(0)
	s_barrier
	s_setprio 1
	s_waitcnt lgkmcnt(0)
	v_mfma_f32_16x16x128_f8f6f4 v[134:137], v[172:179], v[212:219], v[134:137]
	v_mfma_f32_16x16x128_f8f6f4 v[130:133], v[180:187], v[212:219], v[130:133]
	v_mfma_f32_16x16x128_f8f6f4 v[118:121], v[172:179], v[220:227], v[118:121]
	v_mfma_f32_16x16x128_f8f6f4 v[114:117], v[180:187], v[220:227], v[114:117]
	v_mfma_f32_16x16x128_f8f6f4 v[102:105], v[172:179], v[228:235], v[102:105]
	v_mfma_f32_16x16x128_f8f6f4 v[98:101], v[180:187], v[228:235], v[98:101]
	v_mfma_f32_16x16x128_f8f6f4 v[78:81], v[172:179], v[236:243], v[78:81]
	v_mfma_f32_16x16x128_f8f6f4 v[74:77], v[180:187], v[236:243], v[74:77]
	s_setprio 0
	s_setprio 1
	v_mfma_f32_16x16x128_f8f6f4 v[126:129], v[188:195], v[212:219], v[126:129]
	v_mfma_f32_16x16x128_f8f6f4 v[122:125], v[204:211], v[212:219], v[122:125]
	v_mfma_f32_16x16x128_f8f6f4 v[110:113], v[188:195], v[220:227], v[110:113]
	v_mfma_f32_16x16x128_f8f6f4 v[106:109], v[204:211], v[220:227], v[106:109]
	v_mfma_f32_16x16x128_f8f6f4 v[94:97], v[188:195], v[228:235], v[94:97]
	v_mfma_f32_16x16x128_f8f6f4 v[90:93], v[204:211], v[228:235], v[90:93]
	v_mfma_f32_16x16x128_f8f6f4 v[62:65], v[188:195], v[236:243], v[62:65]
	v_mfma_f32_16x16x128_f8f6f4 v[58:61], v[204:211], v[236:243], v[58:61]
	s_setprio 0
	s_barrier
	s_mov_b32 m0, s80
	v_lshl_add_u64 v[196:197], v[150:151], 0, s[26:27]
	s_add_u32 s82, s72, 0x8200
	ds_read_b128 v[212:215], v161 offset:16384
	ds_read_b128 v[216:219], v161 offset:17408
	ds_read_b128 v[220:223], v161 offset:18432
	ds_read_b128 v[224:227], v161 offset:19456
	ds_read_b128 v[228:231], v161 offset:20480
	ds_read_b128 v[232:235], v161 offset:21504
	ds_read_b128 v[236:239], v161 offset:22528
	ds_read_b128 v[240:243], v161 offset:23552
	global_load_lds_dwordx4 v[196:197], off
	v_lshl_add_u64 v[196:197], v[152:153], 0, s[26:27]
	s_mov_b32 m0, s76
	s_addc_u32 s83, s73, 0
	global_load_lds_dwordx4 v[196:197], off
	v_lshl_add_u64 v[196:197], s[82:83], 0, v[140:141]
	s_mov_b32 m0, s77
	s_nop 0
	global_load_lds_dwordx4 v[196:197], off
	v_lshl_add_u64 v[196:197], s[82:83], 0, v[144:145]
	s_mov_b32 m0, s78
	s_nop 0
	global_load_lds_dwordx4 v[196:197], off
	v_lshl_add_u64 v[196:197], v[154:155], 0, s[26:27]
	s_mov_b32 m0, s49
	s_nop 0
	global_load_lds_dwordx4 v[196:197], off
	v_lshl_add_u64 v[196:197], v[156:157], 0, s[26:27]
	s_mov_b32 m0, s51
	s_nop 0
	global_load_lds_dwordx4 v[196:197], off
	s_waitcnt vmcnt(8)
	s_waitcnt lgkmcnt(0)
	s_barrier
	s_setprio 1
	s_waitcnt lgkmcnt(0)
	v_mfma_f32_16x16x128_f8f6f4 v[86:89], v[172:179], v[212:219], v[86:89]
	v_mfma_f32_16x16x128_f8f6f4 v[82:85], v[180:187], v[212:219], v[82:85]
	v_mfma_f32_16x16x128_f8f6f4 v[54:57], v[172:179], v[220:227], v[54:57]
	v_mfma_f32_16x16x128_f8f6f4 v[50:53], v[180:187], v[220:227], v[50:53]
	v_mfma_f32_16x16x128_f8f6f4 v[38:41], v[172:179], v[228:235], v[38:41]
	v_mfma_f32_16x16x128_f8f6f4 v[34:37], v[180:187], v[228:235], v[34:37]
	v_mfma_f32_16x16x128_f8f6f4 v[22:25], v[172:179], v[236:243], v[22:25]
	v_mfma_f32_16x16x128_f8f6f4 v[18:21], v[180:187], v[236:243], v[18:21]
	s_setprio 0
	s_setprio 1
	v_mfma_f32_16x16x128_f8f6f4 v[70:73], v[188:195], v[212:219], v[70:73]
	v_mfma_f32_16x16x128_f8f6f4 v[66:69], v[204:211], v[212:219], v[66:69]
	v_mfma_f32_16x16x128_f8f6f4 v[46:49], v[188:195], v[220:227], v[46:49]
	v_mfma_f32_16x16x128_f8f6f4 v[42:45], v[204:211], v[220:227], v[42:45]
	v_mfma_f32_16x16x128_f8f6f4 v[30:33], v[188:195], v[228:235], v[30:33]
	v_mfma_f32_16x16x128_f8f6f4 v[26:29], v[204:211], v[228:235], v[26:29]
	v_mfma_f32_16x16x128_f8f6f4 v[14:17], v[188:195], v[236:243], v[14:17]
	v_mfma_f32_16x16x128_f8f6f4 v[10:13], v[204:211], v[236:243], v[10:13]
	s_setprio 0
	s_barrier
	ds_read_b128 v[172:175], v158
	ds_read_b128 v[176:179], v158 offset:1024
	ds_read_b128 v[180:183], v158 offset:2048
	ds_read_b128 v[184:187], v158 offset:3072
	ds_read_b128 v[188:191], v159
	ds_read_b128 v[192:195], v159 offset:1024
	ds_read_b128 v[204:207], v159 offset:2048
	ds_read_b128 v[208:211], v159 offset:3072
	s_add_u32 s82, s68, 0x20200
	s_addc_u32 s83, s69, 0
	s_mov_b32 m0, s59
	v_lshl_add_u64 v[196:197], s[82:83], 0, v[138:139]
	ds_read_b128 v[212:215], v161 offset:32768
	ds_read_b128 v[216:219], v161 offset:33792
	ds_read_b128 v[220:223], v161 offset:34816
	ds_read_b128 v[224:227], v161 offset:35840
	ds_read_b128 v[228:231], v161 offset:36864
	ds_read_b128 v[232:235], v161 offset:37888
	ds_read_b128 v[236:239], v161 offset:38912
	ds_read_b128 v[240:243], v161 offset:39936
	global_load_lds_dwordx4 v[196:197], off
	v_lshl_add_u64 v[196:197], s[82:83], 0, v[142:143]
	s_mov_b32 m0, s60
	s_nop 0
	global_load_lds_dwordx4 v[196:197], off
	s_waitcnt vmcnt(8)
	s_waitcnt lgkmcnt(0)
	s_barrier
	s_setprio 1
	s_waitcnt lgkmcnt(0)
	v_mfma_f32_16x16x128_f8f6f4 v[134:137], v[172:179], v[212:219], v[134:137]
	v_mfma_f32_16x16x128_f8f6f4 v[130:133], v[180:187], v[212:219], v[130:133]
	v_mfma_f32_16x16x128_f8f6f4 v[118:121], v[172:179], v[220:227], v[118:121]
	v_mfma_f32_16x16x128_f8f6f4 v[114:117], v[180:187], v[220:227], v[114:117]
	v_mfma_f32_16x16x128_f8f6f4 v[102:105], v[172:179], v[228:235], v[102:105]
	v_mfma_f32_16x16x128_f8f6f4 v[98:101], v[180:187], v[228:235], v[98:101]
	v_mfma_f32_16x16x128_f8f6f4 v[78:81], v[172:179], v[236:243], v[78:81]
	v_mfma_f32_16x16x128_f8f6f4 v[74:77], v[180:187], v[236:243], v[74:77]
	s_setprio 0
	s_setprio 1
	v_mfma_f32_16x16x128_f8f6f4 v[126:129], v[188:195], v[212:219], v[126:129]
	v_mfma_f32_16x16x128_f8f6f4 v[122:125], v[204:211], v[212:219], v[122:125]
	v_mfma_f32_16x16x128_f8f6f4 v[110:113], v[188:195], v[220:227], v[110:113]
	v_mfma_f32_16x16x128_f8f6f4 v[106:109], v[204:211], v[220:227], v[106:109]
	v_mfma_f32_16x16x128_f8f6f4 v[94:97], v[188:195], v[228:235], v[94:97]
	v_mfma_f32_16x16x128_f8f6f4 v[90:93], v[204:211], v[228:235], v[90:93]
	v_mfma_f32_16x16x128_f8f6f4 v[62:65], v[188:195], v[236:243], v[62:65]
	v_mfma_f32_16x16x128_f8f6f4 v[58:61], v[204:211], v[236:243], v[58:61]
	s_setprio 0
	s_barrier
	s_mov_b32 m0, s79
	v_lshl_add_u64 v[196:197], v[150:151], 0, s[28:29]
	s_add_u32 s82, s72, 0x8280
	ds_read_b128 v[212:215], v161 offset:49152
	ds_read_b128 v[216:219], v161 offset:50176
	ds_read_b128 v[220:223], v161 offset:51200
	ds_read_b128 v[224:227], v161 offset:52224
	ds_read_b128 v[228:231], v161 offset:53248
	ds_read_b128 v[232:235], v161 offset:54272
	ds_read_b128 v[236:239], v161 offset:55296
	ds_read_b128 v[240:243], v161 offset:56320
	global_load_lds_dwordx4 v[196:197], off
	v_lshl_add_u64 v[196:197], v[152:153], 0, s[28:29]
	s_mov_b32 m0, s39
	s_addc_u32 s83, s73, 0
	global_load_lds_dwordx4 v[196:197], off
	v_lshl_add_u64 v[196:197], s[82:83], 0, v[140:141]
	s_mov_b32 m0, s41
	s_nop 0
	global_load_lds_dwordx4 v[196:197], off
	v_lshl_add_u64 v[196:197], s[82:83], 0, v[144:145]
	s_mov_b32 m0, s71
	s_nop 0
	global_load_lds_dwordx4 v[196:197], off
	v_lshl_add_u64 v[196:197], v[154:155], 0, s[28:29]
	s_mov_b32 m0, s61
	s_nop 0
	global_load_lds_dwordx4 v[196:197], off
	v_lshl_add_u64 v[196:197], v[156:157], 0, s[28:29]
	s_mov_b32 m0, s62
	s_nop 0
	global_load_lds_dwordx4 v[196:197], off
	s_waitcnt vmcnt(8)
	s_waitcnt lgkmcnt(0)
	s_barrier
	s_setprio 1
	s_waitcnt lgkmcnt(0)
	v_mfma_f32_16x16x128_f8f6f4 v[86:89], v[172:179], v[212:219], v[86:89]
	v_mfma_f32_16x16x128_f8f6f4 v[82:85], v[180:187], v[212:219], v[82:85]
	v_mfma_f32_16x16x128_f8f6f4 v[54:57], v[172:179], v[220:227], v[54:57]
	v_mfma_f32_16x16x128_f8f6f4 v[50:53], v[180:187], v[220:227], v[50:53]
	v_mfma_f32_16x16x128_f8f6f4 v[38:41], v[172:179], v[228:235], v[38:41]
	v_mfma_f32_16x16x128_f8f6f4 v[34:37], v[180:187], v[228:235], v[34:37]
	v_mfma_f32_16x16x128_f8f6f4 v[22:25], v[172:179], v[236:243], v[22:25]
	v_mfma_f32_16x16x128_f8f6f4 v[18:21], v[180:187], v[236:243], v[18:21]
	s_setprio 0
	s_setprio 1
	v_mfma_f32_16x16x128_f8f6f4 v[70:73], v[188:195], v[212:219], v[70:73]
	v_mfma_f32_16x16x128_f8f6f4 v[66:69], v[204:211], v[212:219], v[66:69]
	v_mfma_f32_16x16x128_f8f6f4 v[46:49], v[188:195], v[220:227], v[46:49]
	v_mfma_f32_16x16x128_f8f6f4 v[42:45], v[204:211], v[220:227], v[42:45]
	v_mfma_f32_16x16x128_f8f6f4 v[30:33], v[188:195], v[228:235], v[30:33]
	v_mfma_f32_16x16x128_f8f6f4 v[26:29], v[204:211], v[228:235], v[26:29]
	v_mfma_f32_16x16x128_f8f6f4 v[14:17], v[188:195], v[236:243], v[14:17]
	v_mfma_f32_16x16x128_f8f6f4 v[10:13], v[204:211], v[236:243], v[10:13]
	s_setprio 0
	s_barrier
	ds_read_b128 v[172:175], v162
	ds_read_b128 v[176:179], v162 offset:1024
	ds_read_b128 v[180:183], v162 offset:2048
	ds_read_b128 v[184:187], v162 offset:3072
	ds_read_b128 v[188:191], v163
	ds_read_b128 v[192:195], v163 offset:1024
	ds_read_b128 v[204:207], v163 offset:2048
	ds_read_b128 v[208:211], v163 offset:3072
	s_add_u32 s82, s68, 0x20280
	s_addc_u32 s83, s69, 0
	s_mov_b32 m0, s63
	v_lshl_add_u64 v[196:197], s[82:83], 0, v[138:139]
	ds_read_b128 v[212:215], v161
	ds_read_b128 v[216:219], v161 offset:1024
	ds_read_b128 v[220:223], v161 offset:2048
	ds_read_b128 v[224:227], v161 offset:3072
	ds_read_b128 v[228:231], v161 offset:4096
	ds_read_b128 v[232:235], v161 offset:5120
	ds_read_b128 v[236:239], v161 offset:6144
	ds_read_b128 v[240:243], v161 offset:7168
	global_load_lds_dwordx4 v[196:197], off
	v_lshl_add_u64 v[196:197], s[82:83], 0, v[142:143]
	s_mov_b32 m0, s64
	s_nop 0
	global_load_lds_dwordx4 v[196:197], off
	s_waitcnt vmcnt(8)
	s_waitcnt lgkmcnt(0)
	s_barrier
	s_setprio 1
	s_waitcnt lgkmcnt(0)
	v_mfma_f32_16x16x128_f8f6f4 v[134:137], v[172:179], v[212:219], v[134:137]
	v_mfma_f32_16x16x128_f8f6f4 v[130:133], v[180:187], v[212:219], v[130:133]
	v_mfma_f32_16x16x128_f8f6f4 v[118:121], v[172:179], v[220:227], v[118:121]
	v_mfma_f32_16x16x128_f8f6f4 v[114:117], v[180:187], v[220:227], v[114:117]
	v_mfma_f32_16x16x128_f8f6f4 v[102:105], v[172:179], v[228:235], v[102:105]
	v_mfma_f32_16x16x128_f8f6f4 v[98:101], v[180:187], v[228:235], v[98:101]
	v_mfma_f32_16x16x128_f8f6f4 v[78:81], v[172:179], v[236:243], v[78:81]
	v_mfma_f32_16x16x128_f8f6f4 v[74:77], v[180:187], v[236:243], v[74:77]
	s_setprio 0
	s_setprio 1
	v_mfma_f32_16x16x128_f8f6f4 v[126:129], v[188:195], v[212:219], v[126:129]
	v_mfma_f32_16x16x128_f8f6f4 v[122:125], v[204:211], v[212:219], v[122:125]
	v_mfma_f32_16x16x128_f8f6f4 v[110:113], v[188:195], v[220:227], v[110:113]
	v_mfma_f32_16x16x128_f8f6f4 v[106:109], v[204:211], v[220:227], v[106:109]
	v_mfma_f32_16x16x128_f8f6f4 v[94:97], v[188:195], v[228:235], v[94:97]
	v_mfma_f32_16x16x128_f8f6f4 v[90:93], v[204:211], v[228:235], v[90:93]
	v_mfma_f32_16x16x128_f8f6f4 v[62:65], v[188:195], v[236:243], v[62:65]
	v_mfma_f32_16x16x128_f8f6f4 v[58:61], v[204:211], v[236:243], v[58:61]
	s_setprio 0
	s_barrier
	s_mov_b32 m0, s80
	v_lshl_add_u64 v[196:197], v[150:151], 0, s[30:31]
	s_add_u32 s82, s72, 0x8300
	ds_read_b128 v[212:215], v161 offset:16384
	ds_read_b128 v[216:219], v161 offset:17408
	ds_read_b128 v[220:223], v161 offset:18432
	ds_read_b128 v[224:227], v161 offset:19456
	ds_read_b128 v[228:231], v161 offset:20480
	ds_read_b128 v[232:235], v161 offset:21504
	ds_read_b128 v[236:239], v161 offset:22528
	ds_read_b128 v[240:243], v161 offset:23552
	global_load_lds_dwordx4 v[196:197], off
	v_lshl_add_u64 v[196:197], v[152:153], 0, s[30:31]
	s_mov_b32 m0, s76
	s_addc_u32 s83, s73, 0
	global_load_lds_dwordx4 v[196:197], off
	v_lshl_add_u64 v[196:197], s[82:83], 0, v[140:141]
	s_mov_b32 m0, s77
	s_nop 0
	global_load_lds_dwordx4 v[196:197], off
	v_lshl_add_u64 v[196:197], s[82:83], 0, v[144:145]
	s_mov_b32 m0, s78
	s_nop 0
	global_load_lds_dwordx4 v[196:197], off
	v_lshl_add_u64 v[196:197], v[154:155], 0, s[30:31]
	s_mov_b32 m0, s49
	s_nop 0
	global_load_lds_dwordx4 v[196:197], off
	v_lshl_add_u64 v[196:197], v[156:157], 0, s[30:31]
	s_mov_b32 m0, s51
	s_nop 0
	global_load_lds_dwordx4 v[196:197], off
	s_waitcnt vmcnt(8)
	s_waitcnt lgkmcnt(0)
	s_barrier
	s_setprio 1
	s_waitcnt lgkmcnt(0)
	v_mfma_f32_16x16x128_f8f6f4 v[86:89], v[172:179], v[212:219], v[86:89]
	v_mfma_f32_16x16x128_f8f6f4 v[82:85], v[180:187], v[212:219], v[82:85]
	v_mfma_f32_16x16x128_f8f6f4 v[54:57], v[172:179], v[220:227], v[54:57]
	v_mfma_f32_16x16x128_f8f6f4 v[50:53], v[180:187], v[220:227], v[50:53]
	v_mfma_f32_16x16x128_f8f6f4 v[38:41], v[172:179], v[228:235], v[38:41]
	v_mfma_f32_16x16x128_f8f6f4 v[34:37], v[180:187], v[228:235], v[34:37]
	v_mfma_f32_16x16x128_f8f6f4 v[22:25], v[172:179], v[236:243], v[22:25]
	v_mfma_f32_16x16x128_f8f6f4 v[18:21], v[180:187], v[236:243], v[18:21]
	s_setprio 0
	s_setprio 1
	v_mfma_f32_16x16x128_f8f6f4 v[70:73], v[188:195], v[212:219], v[70:73]
	v_mfma_f32_16x16x128_f8f6f4 v[66:69], v[204:211], v[212:219], v[66:69]
	v_mfma_f32_16x16x128_f8f6f4 v[46:49], v[188:195], v[220:227], v[46:49]
	v_mfma_f32_16x16x128_f8f6f4 v[42:45], v[204:211], v[220:227], v[42:45]
	v_mfma_f32_16x16x128_f8f6f4 v[30:33], v[188:195], v[228:235], v[30:33]
	v_mfma_f32_16x16x128_f8f6f4 v[26:29], v[204:211], v[228:235], v[26:29]
	v_mfma_f32_16x16x128_f8f6f4 v[14:17], v[188:195], v[236:243], v[14:17]
	v_mfma_f32_16x16x128_f8f6f4 v[10:13], v[204:211], v[236:243], v[10:13]
	s_setprio 0
	s_barrier
	ds_read_b128 v[172:175], v158
	ds_read_b128 v[176:179], v158 offset:1024
	ds_read_b128 v[180:183], v158 offset:2048
	ds_read_b128 v[184:187], v158 offset:3072
	ds_read_b128 v[188:191], v159
	ds_read_b128 v[192:195], v159 offset:1024
	ds_read_b128 v[204:207], v159 offset:2048
	ds_read_b128 v[208:211], v159 offset:3072
	s_add_u32 s82, s68, 0x20300
	s_addc_u32 s83, s69, 0
	s_mov_b32 m0, s59
	v_lshl_add_u64 v[196:197], s[82:83], 0, v[138:139]
	ds_read_b128 v[212:215], v161 offset:32768
	ds_read_b128 v[216:219], v161 offset:33792
	ds_read_b128 v[220:223], v161 offset:34816
	ds_read_b128 v[224:227], v161 offset:35840
	ds_read_b128 v[228:231], v161 offset:36864
	ds_read_b128 v[232:235], v161 offset:37888
	ds_read_b128 v[236:239], v161 offset:38912
	ds_read_b128 v[240:243], v161 offset:39936
	global_load_lds_dwordx4 v[196:197], off
	v_lshl_add_u64 v[196:197], s[82:83], 0, v[142:143]
	s_mov_b32 m0, s60
	s_nop 0
	global_load_lds_dwordx4 v[196:197], off
	s_waitcnt vmcnt(8)
	s_waitcnt lgkmcnt(0)
	s_barrier
	s_setprio 1
	s_waitcnt lgkmcnt(0)
	v_mfma_f32_16x16x128_f8f6f4 v[134:137], v[172:179], v[212:219], v[134:137]
	v_mfma_f32_16x16x128_f8f6f4 v[130:133], v[180:187], v[212:219], v[130:133]
	v_mfma_f32_16x16x128_f8f6f4 v[118:121], v[172:179], v[220:227], v[118:121]
	v_mfma_f32_16x16x128_f8f6f4 v[114:117], v[180:187], v[220:227], v[114:117]
	v_mfma_f32_16x16x128_f8f6f4 v[102:105], v[172:179], v[228:235], v[102:105]
	v_mfma_f32_16x16x128_f8f6f4 v[98:101], v[180:187], v[228:235], v[98:101]
	v_mfma_f32_16x16x128_f8f6f4 v[78:81], v[172:179], v[236:243], v[78:81]
	v_mfma_f32_16x16x128_f8f6f4 v[74:77], v[180:187], v[236:243], v[74:77]
	s_setprio 0
	s_setprio 1
	v_mfma_f32_16x16x128_f8f6f4 v[126:129], v[188:195], v[212:219], v[126:129]
	v_mfma_f32_16x16x128_f8f6f4 v[122:125], v[204:211], v[212:219], v[122:125]
	v_mfma_f32_16x16x128_f8f6f4 v[110:113], v[188:195], v[220:227], v[110:113]
	v_mfma_f32_16x16x128_f8f6f4 v[106:109], v[204:211], v[220:227], v[106:109]
	v_mfma_f32_16x16x128_f8f6f4 v[94:97], v[188:195], v[228:235], v[94:97]
	v_mfma_f32_16x16x128_f8f6f4 v[90:93], v[204:211], v[228:235], v[90:93]
	v_mfma_f32_16x16x128_f8f6f4 v[62:65], v[188:195], v[236:243], v[62:65]
	v_mfma_f32_16x16x128_f8f6f4 v[58:61], v[204:211], v[236:243], v[58:61]
	s_setprio 0
	s_barrier
	s_mov_b32 m0, s79
	v_lshl_add_u64 v[150:151], v[150:151], 0, s[34:35]
	s_add_u32 s72, s72, 0x8380
	ds_read_b128 v[212:215], v161 offset:49152
	ds_read_b128 v[216:219], v161 offset:50176
	ds_read_b128 v[220:223], v161 offset:51200
	ds_read_b128 v[224:227], v161 offset:52224
	ds_read_b128 v[228:231], v161 offset:53248
	ds_read_b128 v[232:235], v161 offset:54272
	ds_read_b128 v[236:239], v161 offset:55296
	ds_read_b128 v[240:243], v161 offset:56320
	global_load_lds_dwordx4 v[150:151], off
	v_lshl_add_u64 v[150:151], v[152:153], 0, s[34:35]
	s_mov_b32 m0, s39
	s_addc_u32 s73, s73, 0
	global_load_lds_dwordx4 v[150:151], off
	v_lshl_add_u64 v[150:151], s[72:73], 0, v[140:141]
	s_mov_b32 m0, s41
	s_nop 0
	global_load_lds_dwordx4 v[150:151], off
	v_lshl_add_u64 v[150:151], s[72:73], 0, v[144:145]
	s_mov_b32 m0, s71
	s_nop 0
	global_load_lds_dwordx4 v[150:151], off
	v_lshl_add_u64 v[150:151], v[154:155], 0, s[34:35]
	s_mov_b32 m0, s61
	s_nop 0
	global_load_lds_dwordx4 v[150:151], off
	v_lshl_add_u64 v[150:151], v[156:157], 0, s[34:35]
	s_mov_b32 m0, s62
	s_nop 0
	global_load_lds_dwordx4 v[150:151], off
	s_waitcnt vmcnt(8)
	s_waitcnt lgkmcnt(0)
	s_barrier
	s_setprio 1
	s_waitcnt lgkmcnt(0)
	v_mfma_f32_16x16x128_f8f6f4 v[86:89], v[172:179], v[212:219], v[86:89]
	v_mfma_f32_16x16x128_f8f6f4 v[82:85], v[180:187], v[212:219], v[82:85]
	v_mfma_f32_16x16x128_f8f6f4 v[54:57], v[172:179], v[220:227], v[54:57]
	v_mfma_f32_16x16x128_f8f6f4 v[50:53], v[180:187], v[220:227], v[50:53]
	v_mfma_f32_16x16x128_f8f6f4 v[38:41], v[172:179], v[228:235], v[38:41]
	v_mfma_f32_16x16x128_f8f6f4 v[34:37], v[180:187], v[228:235], v[34:37]
	v_mfma_f32_16x16x128_f8f6f4 v[22:25], v[172:179], v[236:243], v[22:25]
	v_mfma_f32_16x16x128_f8f6f4 v[18:21], v[180:187], v[236:243], v[18:21]
	s_setprio 0
	s_setprio 1
	v_mfma_f32_16x16x128_f8f6f4 v[70:73], v[188:195], v[212:219], v[70:73]
	v_mfma_f32_16x16x128_f8f6f4 v[66:69], v[204:211], v[212:219], v[66:69]
	v_mfma_f32_16x16x128_f8f6f4 v[46:49], v[188:195], v[220:227], v[46:49]
	v_mfma_f32_16x16x128_f8f6f4 v[42:45], v[204:211], v[220:227], v[42:45]
	v_mfma_f32_16x16x128_f8f6f4 v[30:33], v[188:195], v[228:235], v[30:33]
	v_mfma_f32_16x16x128_f8f6f4 v[26:29], v[204:211], v[228:235], v[26:29]
	v_mfma_f32_16x16x128_f8f6f4 v[14:17], v[188:195], v[236:243], v[14:17]
	v_mfma_f32_16x16x128_f8f6f4 v[10:13], v[204:211], v[236:243], v[10:13]
	s_setprio 0
	s_barrier
	ds_read_b128 v[150:153], v162
	ds_read_b128 v[154:157], v162 offset:1024
	ds_read_b128 v[172:175], v162 offset:2048
	ds_read_b128 v[176:179], v162 offset:3072
	ds_read_b128 v[180:183], v163
	ds_read_b128 v[184:187], v163 offset:1024
	ds_read_b128 v[188:191], v163 offset:2048
	ds_read_b128 v[192:195], v163 offset:3072
	s_add_u32 s68, s68, 0x20380
	s_addc_u32 s69, s69, 0
	s_mov_b32 m0, s63
	v_lshl_add_u64 v[196:197], s[68:69], 0, v[138:139]
	ds_read_b128 v[204:207], v161
	ds_read_b128 v[208:211], v161 offset:1024
	ds_read_b128 v[212:215], v161 offset:2048
	ds_read_b128 v[216:219], v161 offset:3072
	ds_read_b128 v[220:223], v161 offset:4096
	ds_read_b128 v[224:227], v161 offset:5120
	ds_read_b128 v[228:231], v161 offset:6144
	ds_read_b128 v[232:235], v161 offset:7168
	global_load_lds_dwordx4 v[196:197], off
	v_lshl_add_u64 v[196:197], s[68:69], 0, v[142:143]
	s_mov_b32 m0, s64
	s_nop 0
	global_load_lds_dwordx4 v[196:197], off
	s_waitcnt vmcnt(8)
	s_waitcnt lgkmcnt(0)
	s_barrier
	s_setprio 1
	s_waitcnt lgkmcnt(0)
	v_mfma_f32_16x16x128_f8f6f4 v[134:137], v[150:157], v[204:211], v[134:137]
	v_mfma_f32_16x16x128_f8f6f4 v[130:133], v[172:179], v[204:211], v[130:133]
	v_mfma_f32_16x16x128_f8f6f4 v[118:121], v[150:157], v[212:219], v[118:121]
	v_mfma_f32_16x16x128_f8f6f4 v[114:117], v[172:179], v[212:219], v[114:117]
	v_mfma_f32_16x16x128_f8f6f4 v[102:105], v[150:157], v[220:227], v[102:105]
	v_mfma_f32_16x16x128_f8f6f4 v[98:101], v[172:179], v[220:227], v[98:101]
	v_mfma_f32_16x16x128_f8f6f4 v[78:81], v[150:157], v[228:235], v[78:81]
	v_mfma_f32_16x16x128_f8f6f4 v[74:77], v[172:179], v[228:235], v[74:77]
	s_setprio 0
	s_setprio 1
	v_mfma_f32_16x16x128_f8f6f4 v[126:129], v[180:187], v[204:211], v[126:129]
	v_mfma_f32_16x16x128_f8f6f4 v[122:125], v[188:195], v[204:211], v[122:125]
	v_mfma_f32_16x16x128_f8f6f4 v[110:113], v[180:187], v[212:219], v[110:113]
	v_mfma_f32_16x16x128_f8f6f4 v[106:109], v[188:195], v[212:219], v[106:109]
	v_mfma_f32_16x16x128_f8f6f4 v[94:97], v[180:187], v[220:227], v[94:97]
	v_mfma_f32_16x16x128_f8f6f4 v[90:93], v[188:195], v[220:227], v[90:93]
	v_mfma_f32_16x16x128_f8f6f4 v[62:65], v[180:187], v[228:235], v[62:65]
	v_mfma_f32_16x16x128_f8f6f4 v[58:61], v[188:195], v[228:235], v[58:61]
	s_setprio 0
	s_barrier
	s_mov_b32 m0, s80
	v_lshl_add_u64 v[196:197], s[8:9], 0, v[140:141]
	s_add_u32 s68, s8, 0x8000
	ds_read_b128 v[204:207], v161 offset:16384
	ds_read_b128 v[208:211], v161 offset:17408
	ds_read_b128 v[212:215], v161 offset:18432
	ds_read_b128 v[216:219], v161 offset:19456
	ds_read_b128 v[220:223], v161 offset:20480
	ds_read_b128 v[224:227], v161 offset:21504
	ds_read_b128 v[228:231], v161 offset:22528
	ds_read_b128 v[232:235], v161 offset:23552
	global_load_lds_dwordx4 v[196:197], off
	v_lshl_add_u64 v[198:199], s[8:9], 0, v[144:145]
	s_mov_b32 m0, s76
	s_addc_u32 s69, s9, 0
	global_load_lds_dwordx4 v[198:199], off
	v_lshl_add_u64 v[200:201], s[68:69], 0, v[140:141]
	s_mov_b32 m0, s77
	v_lshl_add_u64 v[236:237], s[74:75], 0, v[142:143]
	global_load_lds_dwordx4 v[200:201], off
	v_lshl_add_u64 v[200:201], s[68:69], 0, v[144:145]
	s_mov_b32 m0, s78
	s_nop 0
	global_load_lds_dwordx4 v[200:201], off
	v_lshl_add_u64 v[200:201], s[74:75], 0, v[138:139]
	s_mov_b32 m0, s49
	s_nop 0
	global_load_lds_dwordx4 v[200:201], off
	s_mov_b32 m0, s51
	s_nop 0
	global_load_lds_dwordx4 v[236:237], off
	s_waitcnt vmcnt(8)
	s_waitcnt lgkmcnt(0)
	s_barrier
	s_setprio 1
	s_waitcnt lgkmcnt(0)
	v_mfma_f32_16x16x128_f8f6f4 v[86:89], v[150:157], v[204:211], v[86:89]
	v_mfma_f32_16x16x128_f8f6f4 v[82:85], v[172:179], v[204:211], v[82:85]
	v_mfma_f32_16x16x128_f8f6f4 v[54:57], v[150:157], v[212:219], v[54:57]
	v_mfma_f32_16x16x128_f8f6f4 v[50:53], v[172:179], v[212:219], v[50:53]
	v_mfma_f32_16x16x128_f8f6f4 v[38:41], v[150:157], v[220:227], v[38:41]
	v_mfma_f32_16x16x128_f8f6f4 v[34:37], v[172:179], v[220:227], v[34:37]
	v_mfma_f32_16x16x128_f8f6f4 v[22:25], v[150:157], v[228:235], v[22:25]
	v_mfma_f32_16x16x128_f8f6f4 v[18:21], v[172:179], v[228:235], v[18:21]
	s_setprio 0
	s_setprio 1
	v_mfma_f32_16x16x128_f8f6f4 v[70:73], v[180:187], v[204:211], v[70:73]
	v_mfma_f32_16x16x128_f8f6f4 v[66:69], v[188:195], v[204:211], v[66:69]
	v_mfma_f32_16x16x128_f8f6f4 v[46:49], v[180:187], v[212:219], v[46:49]
	v_mfma_f32_16x16x128_f8f6f4 v[42:45], v[188:195], v[212:219], v[42:45]
	v_mfma_f32_16x16x128_f8f6f4 v[30:33], v[180:187], v[220:227], v[30:33]
	v_mfma_f32_16x16x128_f8f6f4 v[26:29], v[188:195], v[220:227], v[26:29]
	v_mfma_f32_16x16x128_f8f6f4 v[14:17], v[180:187], v[228:235], v[14:17]
	v_mfma_f32_16x16x128_f8f6f4 v[10:13], v[188:195], v[228:235], v[10:13]
	s_setprio 0
	s_barrier
	ds_read_b128 v[150:153], v158
	ds_read_b128 v[154:157], v158 offset:1024
	ds_read_b128 v[172:175], v158 offset:2048
	ds_read_b128 v[176:179], v158 offset:3072
	ds_read_b128 v[180:183], v159
	ds_read_b128 v[184:187], v159 offset:1024
	ds_read_b128 v[188:191], v159 offset:2048
	ds_read_b128 v[192:195], v159 offset:3072
	s_add_u32 s68, s74, 0x20000
	s_addc_u32 s69, s75, 0
	s_mov_b32 m0, s59
	v_lshl_add_u64 v[158:159], s[68:69], 0, v[138:139]
	ds_read_b128 v[204:207], v161 offset:32768
	ds_read_b128 v[208:211], v161 offset:33792
	ds_read_b128 v[212:215], v161 offset:34816
	ds_read_b128 v[216:219], v161 offset:35840
	ds_read_b128 v[220:223], v161 offset:36864
	ds_read_b128 v[224:227], v161 offset:37888
	ds_read_b128 v[228:231], v161 offset:38912
	ds_read_b128 v[232:235], v161 offset:39936
	global_load_lds_dwordx4 v[158:159], off
	v_lshl_add_u64 v[158:159], s[68:69], 0, v[142:143]
	s_mov_b32 m0, s60
	s_nop 0
	global_load_lds_dwordx4 v[158:159], off
	s_waitcnt vmcnt(8)
	s_waitcnt lgkmcnt(0)
	s_barrier
	s_setprio 1
	s_waitcnt lgkmcnt(0)
	v_mfma_f32_16x16x128_f8f6f4 v[134:137], v[150:157], v[204:211], v[134:137]
	v_mfma_f32_16x16x128_f8f6f4 v[130:133], v[172:179], v[204:211], v[130:133]
	v_mfma_f32_16x16x128_f8f6f4 v[118:121], v[150:157], v[212:219], v[118:121]
	v_mfma_f32_16x16x128_f8f6f4 v[114:117], v[172:179], v[212:219], v[114:117]
	v_mfma_f32_16x16x128_f8f6f4 v[102:105], v[150:157], v[220:227], v[102:105]
	v_mfma_f32_16x16x128_f8f6f4 v[98:101], v[172:179], v[220:227], v[98:101]
	v_mfma_f32_16x16x128_f8f6f4 v[78:81], v[150:157], v[228:235], v[78:81]
	v_mfma_f32_16x16x128_f8f6f4 v[74:77], v[172:179], v[228:235], v[74:77]
	s_setprio 0
	s_setprio 1
	v_mfma_f32_16x16x128_f8f6f4 v[126:129], v[180:187], v[204:211], v[126:129]
	v_mfma_f32_16x16x128_f8f6f4 v[122:125], v[188:195], v[204:211], v[122:125]
	v_mfma_f32_16x16x128_f8f6f4 v[110:113], v[180:187], v[212:219], v[110:113]
	v_mfma_f32_16x16x128_f8f6f4 v[106:109], v[188:195], v[212:219], v[106:109]
	v_mfma_f32_16x16x128_f8f6f4 v[94:97], v[180:187], v[220:227], v[94:97]
	v_mfma_f32_16x16x128_f8f6f4 v[90:93], v[188:195], v[220:227], v[90:93]
	v_mfma_f32_16x16x128_f8f6f4 v[62:65], v[180:187], v[228:235], v[62:65]
	v_mfma_f32_16x16x128_f8f6f4 v[58:61], v[188:195], v[228:235], v[58:61]
	s_setprio 0
	s_barrier
	s_mov_b32 m0, s79
	v_lshl_add_u64 v[158:159], v[196:197], 0, s[18:19]
	s_add_u32 s8, s8, 0x8080
	ds_read_b128 v[204:207], v161 offset:49152
	ds_read_b128 v[208:211], v161 offset:50176
	ds_read_b128 v[212:215], v161 offset:51200
	ds_read_b128 v[216:219], v161 offset:52224
	ds_read_b128 v[220:223], v161 offset:53248
	ds_read_b128 v[224:227], v161 offset:54272
	ds_read_b128 v[228:231], v161 offset:55296
	ds_read_b128 v[232:235], v161 offset:56320
	global_load_lds_dwordx4 v[158:159], off
	v_lshl_add_u64 v[158:159], v[198:199], 0, s[18:19]
	s_mov_b32 m0, s39
	s_addc_u32 s9, s9, 0
	global_load_lds_dwordx4 v[158:159], off
	v_lshl_add_u64 v[158:159], s[8:9], 0, v[140:141]
	s_mov_b32 m0, s41
	s_nop 0
	global_load_lds_dwordx4 v[158:159], off
	v_lshl_add_u64 v[158:159], s[8:9], 0, v[144:145]
	s_mov_b32 m0, s71
	s_nop 0
	global_load_lds_dwordx4 v[158:159], off
	v_lshl_add_u64 v[158:159], v[200:201], 0, s[18:19]
	s_mov_b32 m0, s61
	s_nop 0
	global_load_lds_dwordx4 v[158:159], off
	v_lshl_add_u64 v[158:159], v[236:237], 0, s[18:19]
	s_mov_b32 m0, s62
	s_nop 0
	global_load_lds_dwordx4 v[158:159], off
	s_waitcnt vmcnt(8)
	s_waitcnt lgkmcnt(0)
	s_barrier
	s_setprio 1
	s_waitcnt lgkmcnt(0)
	v_mfma_f32_16x16x128_f8f6f4 v[86:89], v[150:157], v[204:211], v[86:89]
	v_mfma_f32_16x16x128_f8f6f4 v[82:85], v[172:179], v[204:211], v[82:85]
	v_mfma_f32_16x16x128_f8f6f4 v[54:57], v[150:157], v[212:219], v[54:57]
	v_mfma_f32_16x16x128_f8f6f4 v[50:53], v[172:179], v[212:219], v[50:53]
	v_mfma_f32_16x16x128_f8f6f4 v[38:41], v[150:157], v[220:227], v[38:41]
	v_mfma_f32_16x16x128_f8f6f4 v[34:37], v[172:179], v[220:227], v[34:37]
	v_mfma_f32_16x16x128_f8f6f4 v[22:25], v[150:157], v[228:235], v[22:25]
	v_mfma_f32_16x16x128_f8f6f4 v[18:21], v[172:179], v[228:235], v[18:21]
	s_setprio 0
	s_setprio 1
	v_mfma_f32_16x16x128_f8f6f4 v[70:73], v[180:187], v[204:211], v[70:73]
	v_mfma_f32_16x16x128_f8f6f4 v[66:69], v[188:195], v[204:211], v[66:69]
	v_mfma_f32_16x16x128_f8f6f4 v[46:49], v[180:187], v[212:219], v[46:49]
	v_mfma_f32_16x16x128_f8f6f4 v[42:45], v[188:195], v[212:219], v[42:45]
	v_mfma_f32_16x16x128_f8f6f4 v[30:33], v[180:187], v[220:227], v[30:33]
	v_mfma_f32_16x16x128_f8f6f4 v[26:29], v[188:195], v[220:227], v[26:29]
	v_mfma_f32_16x16x128_f8f6f4 v[14:17], v[180:187], v[228:235], v[14:17]
	v_mfma_f32_16x16x128_f8f6f4 v[10:13], v[188:195], v[228:235], v[10:13]
	s_setprio 0
	s_barrier
	s_andn2_b64 s[8:9], exec, s[6:7]
	s_andn2_b64 vcc, exec, s[6:7]
	s_cbranch_vccnz .LBB0_1625
	s_add_u32 s6, s44, 0x20080
	s_addc_u32 s7, s45, 0
	s_mov_b32 m0, s63
	v_lshl_add_u64 v[150:151], s[6:7], 0, v[138:139]
	v_lshl_add_u64 v[152:153], s[6:7], 0, v[142:143]
	global_load_lds_dwordx4 v[150:151], off
	s_mov_b32 m0, s64
	s_nop 0
	global_load_lds_dwordx4 v[152:153], off

.LBB0_3342:
	s_nop 0
	s_andn2_b64 s[8:9], exec, s[10:11]
	s_andn2_b64 vcc, exec, s[10:11]
	v_mov_b32_e32 v148, v150
	v_mov_b32_e32 v146, v152
	v_mov_b32_e32 v173, v154
	v_mov_b32_e32 v172, v142
	s_cbranch_vccnz .LBB0_3344
	s_ashr_i32 s67, s66, 31
	s_lshl_b64 s[72:73], s[66:67], 10
	s_add_u32 s72, s4, s72
	s_addc_u32 s73, s5, s73
	global_load_dword v200, v1, s[72:73]
	global_load_dword v201, v162, s[72:73]
	global_load_dword v252, v162, s[72:73] offset:512
	global_load_dword v253, v1, s[72:73] offset:512

.LBB0_3425:
	s_ashr_i32 s43, s42, 31
	s_lshl_b64 s[10:11], s[42:43], 18
	s_add_u32 s46, s6, s10
	ds_read_b128 v[10:13], v162
	ds_read_b128 v[14:17], v162 offset:1024
	ds_read_b128 v[26:29], v162 offset:2048
	ds_read_b128 v[30:33], v162 offset:3072
	ds_read_b128 v[172:175], v163
	ds_read_b128 v[176:179], v163 offset:1024
	ds_read_b128 v[180:183], v163 offset:2048
	ds_read_b128 v[184:187], v163 offset:3072
	s_addc_u32 s47, s7, s11
	s_and_b64 s[10:11], s[8:9], exec
	s_cselect_b32 s71, s47, s65
	s_cselect_b32 s70, s46, s64
	s_ashr_i32 s45, s44, 31
	s_ashr_i32 s41, s40, 31
	s_lshl_b64 s[10:11], s[44:45], 20
	s_lshl_b64 s[48:49], s[40:41], 18
	s_add_u32 s10, s33, s10
	s_addc_u32 s11, s39, s11
	s_add_u32 s48, s10, s48
	s_addc_u32 s49, s11, s49
	s_and_b64 s[10:11], s[8:9], exec
	s_cselect_b32 s11, s49, s67
	s_cselect_b32 s10, s48, s66
	ds_read_b128 v[18:21], v161
	ds_read_b128 v[22:25], v161 offset:1024
	ds_read_b128 v[34:37], v161 offset:2048
	ds_read_b128 v[38:41], v161 offset:3072
	ds_read_b128 v[42:45], v161 offset:4096
	ds_read_b128 v[46:49], v161 offset:5120
	ds_read_b128 v[50:53], v161 offset:6144
	ds_read_b128 v[54:57], v161 offset:7168
	s_waitcnt vmcnt(16)
	s_waitcnt lgkmcnt(0)
	s_barrier
	s_setprio 1
	s_waitcnt lgkmcnt(0)
	v_mfma_f32_16x16x128_f8f6f4 v[134:137], v[10:17], v[18:25], 0
	v_mfma_f32_16x16x128_f8f6f4 v[130:133], v[26:33], v[18:25], 0
	v_mfma_f32_16x16x128_f8f6f4 v[118:121], v[10:17], v[34:41], 0
	v_mfma_f32_16x16x128_f8f6f4 v[114:117], v[26:33], v[34:41], 0
	v_mfma_f32_16x16x128_f8f6f4 v[102:105], v[10:17], v[42:49], 0
	v_mfma_f32_16x16x128_f8f6f4 v[98:101], v[26:33], v[42:49], 0
	v_mfma_f32_16x16x128_f8f6f4 v[78:81], v[10:17], v[50:57], 0
	v_mfma_f32_16x16x128_f8f6f4 v[74:77], v[26:33], v[50:57], 0
	s_setprio 0
	s_setprio 1
	v_mfma_f32_16x16x128_f8f6f4 v[126:129], v[172:179], v[18:25], 0
	v_mfma_f32_16x16x128_f8f6f4 v[122:125], v[180:187], v[18:25], 0
	v_mfma_f32_16x16x128_f8f6f4 v[110:113], v[172:179], v[34:41], 0
	v_mfma_f32_16x16x128_f8f6f4 v[106:109], v[180:187], v[34:41], 0
	v_mfma_f32_16x16x128_f8f6f4 v[94:97], v[172:179], v[42:49], 0
	v_mfma_f32_16x16x128_f8f6f4 v[90:93], v[180:187], v[42:49], 0
	v_mfma_f32_16x16x128_f8f6f4 v[62:65], v[172:179], v[50:57], 0
	v_mfma_f32_16x16x128_f8f6f4 v[58:61], v[180:187], v[50:57], 0
	s_setprio 0
	s_barrier
	s_add_i32 s80, s73, s56
	v_lshl_add_u64 v[150:151], s[66:67], 0, v[140:141]
	s_add_i32 s76, s80, 0x2000
	v_lshl_add_u64 v[18:19], v[150:151], 0, s[24:25]
	s_mov_b32 m0, s80
	v_lshl_add_u64 v[152:153], s[66:67], 0, v[144:145]
	s_add_u32 s78, s66, 0x8100
	ds_read_b128 v[42:45], v161 offset:16384
	ds_read_b128 v[46:49], v161 offset:17408
	ds_read_b128 v[188:191], v161 offset:18432
	ds_read_b128 v[192:195], v161 offset:19456
	ds_read_b128 v[204:207], v161 offset:20480
	ds_read_b128 v[208:211], v161 offset:21504
	ds_read_b128 v[212:215], v161 offset:22528
	ds_read_b128 v[216:219], v161 offset:23552
	global_load_lds_dwordx4 v[18:19], off
	v_lshl_add_u64 v[18:19], v[152:153], 0, s[24:25]
	s_mov_b32 m0, s76
	s_addc_u32 s79, s67, 0
	s_add_i32 s77, s74, s56
	global_load_lds_dwordx4 v[18:19], off
	v_lshl_add_u64 v[18:19], s[78:79], 0, v[140:141]
	s_mov_b32 m0, s77
	v_lshl_add_u64 v[154:155], s[64:65], 0, v[138:139]
	global_load_lds_dwordx4 v[18:19], off
	v_lshl_add_u64 v[18:19], s[78:79], 0, v[144:145]
	s_add_i32 s78, s77, 0x2000
	s_mov_b32 m0, s78
	v_lshl_add_u64 v[156:157], s[64:65], 0, v[142:143]
	global_load_lds_dwordx4 v[18:19], off
	v_lshl_add_u64 v[18:19], v[154:155], 0, s[24:25]
	s_mov_b32 m0, s51
	s_nop 0
	global_load_lds_dwordx4 v[18:19], off
	v_lshl_add_u64 v[18:19], v[156:157], 0, s[24:25]
	s_mov_b32 m0, s57
	s_nop 0
	global_load_lds_dwordx4 v[18:19], off
	s_waitcnt vmcnt(16)
	s_waitcnt lgkmcnt(0)
	s_barrier
	s_setprio 1
	s_waitcnt lgkmcnt(0)
	v_mfma_f32_16x16x128_f8f6f4 v[86:89], v[10:17], v[42:49], 0
	v_mfma_f32_16x16x128_f8f6f4 v[82:85], v[26:33], v[42:49], 0
	v_mfma_f32_16x16x128_f8f6f4 v[54:57], v[10:17], v[188:195], 0
	v_mfma_f32_16x16x128_f8f6f4 v[50:53], v[26:33], v[188:195], 0
	v_mfma_f32_16x16x128_f8f6f4 v[38:41], v[10:17], v[204:211], 0
	v_mfma_f32_16x16x128_f8f6f4 v[34:37], v[26:33], v[204:211], 0
	v_mfma_f32_16x16x128_f8f6f4 v[22:25], v[10:17], v[212:219], 0
	v_mfma_f32_16x16x128_f8f6f4 v[18:21], v[26:33], v[212:219], 0
	s_setprio 0
	s_setprio 1
	v_mfma_f32_16x16x128_f8f6f4 v[70:73], v[172:179], v[42:49], 0
	v_mfma_f32_16x16x128_f8f6f4 v[66:69], v[180:187], v[42:49], 0
	v_mfma_f32_16x16x128_f8f6f4 v[46:49], v[172:179], v[188:195], 0
	v_mfma_f32_16x16x128_f8f6f4 v[42:45], v[180:187], v[188:195], 0
	v_mfma_f32_16x16x128_f8f6f4 v[30:33], v[172:179], v[204:211], 0
	v_mfma_f32_16x16x128_f8f6f4 v[26:29], v[180:187], v[204:211], 0
	v_mfma_f32_16x16x128_f8f6f4 v[14:17], v[172:179], v[212:219], 0
	v_mfma_f32_16x16x128_f8f6f4 v[10:13], v[180:187], v[212:219], 0
	s_setprio 0
	s_barrier
	s_add_i32 s79, 0, 0x18000
	s_add_i32 s43, 0, 0x1c000
	v_add_u32_e32 v158, s79, v160
	v_add_u32_e32 v159, s43, v160
	ds_read_b128 v[172:175], v158
	ds_read_b128 v[176:179], v158 offset:1024
	ds_read_b128 v[180:183], v158 offset:2048
	ds_read_b128 v[184:187], v158 offset:3072
	ds_read_b128 v[188:191], v159
	ds_read_b128 v[192:195], v159 offset:1024
	ds_read_b128 v[204:207], v159 offset:2048
	ds_read_b128 v[208:211], v159 offset:3072
	s_add_u32 s82, s64, 0x20100
	s_addc_u32 s83, s65, 0
	s_mov_b32 m0, s58
	v_lshl_add_u64 v[196:197], s[82:83], 0, v[138:139]
	ds_read_b128 v[212:215], v161 offset:32768
	ds_read_b128 v[216:219], v161 offset:33792
	ds_read_b128 v[220:223], v161 offset:34816
	ds_read_b128 v[224:227], v161 offset:35840
	ds_read_b128 v[228:231], v161 offset:36864
	ds_read_b128 v[232:235], v161 offset:37888
	ds_read_b128 v[236:239], v161 offset:38912
	ds_read_b128 v[240:243], v161 offset:39936
	global_load_lds_dwordx4 v[196:197], off
	v_lshl_add_u64 v[196:197], s[82:83], 0, v[142:143]
	s_mov_b32 m0, s59
	s_nop 0
	global_load_lds_dwordx4 v[196:197], off
	s_waitcnt vmcnt(16)
	s_waitcnt lgkmcnt(0)
	s_barrier
	s_setprio 1
	s_waitcnt lgkmcnt(0)
	v_mfma_f32_16x16x128_f8f6f4 v[134:137], v[172:179], v[212:219], v[134:137]
	v_mfma_f32_16x16x128_f8f6f4 v[130:133], v[180:187], v[212:219], v[130:133]
	v_mfma_f32_16x16x128_f8f6f4 v[118:121], v[172:179], v[220:227], v[118:121]
	v_mfma_f32_16x16x128_f8f6f4 v[114:117], v[180:187], v[220:227], v[114:117]
	v_mfma_f32_16x16x128_f8f6f4 v[102:105], v[172:179], v[228:235], v[102:105]
	v_mfma_f32_16x16x128_f8f6f4 v[98:101], v[180:187], v[228:235], v[98:101]
	v_mfma_f32_16x16x128_f8f6f4 v[78:81], v[172:179], v[236:243], v[78:81]
	v_mfma_f32_16x16x128_f8f6f4 v[74:77], v[180:187], v[236:243], v[74:77]
	s_setprio 0
	s_setprio 1
	v_mfma_f32_16x16x128_f8f6f4 v[126:129], v[188:195], v[212:219], v[126:129]
	v_mfma_f32_16x16x128_f8f6f4 v[122:125], v[204:211], v[212:219], v[122:125]
	v_mfma_f32_16x16x128_f8f6f4 v[110:113], v[188:195], v[220:227], v[110:113]
	v_mfma_f32_16x16x128_f8f6f4 v[106:109], v[204:211], v[220:227], v[106:109]
	v_mfma_f32_16x16x128_f8f6f4 v[94:97], v[188:195], v[228:235], v[94:97]
	v_mfma_f32_16x16x128_f8f6f4 v[90:93], v[204:211], v[228:235], v[90:93]
	v_mfma_f32_16x16x128_f8f6f4 v[62:65], v[188:195], v[236:243], v[62:65]
	v_mfma_f32_16x16x128_f8f6f4 v[58:61], v[204:211], v[236:243], v[58:61]
	s_setprio 0
	s_barrier
	s_add_i32 s79, s79, s56
	s_add_i32 s41, s79, 0x2000
	v_lshl_add_u64 v[196:197], v[150:151], 0, s[26:27]
	s_mov_b32 m0, s79
	s_add_u32 s82, s66, 0x8180
	ds_read_b128 v[212:215], v161 offset:49152
	ds_read_b128 v[216:219], v161 offset:50176
	ds_read_b128 v[220:223], v161 offset:51200
	ds_read_b128 v[224:227], v161 offset:52224
	ds_read_b128 v[228:231], v161 offset:53248
	ds_read_b128 v[232:235], v161 offset:54272
	ds_read_b128 v[236:239], v161 offset:55296
	ds_read_b128 v[240:243], v161 offset:56320
	global_load_lds_dwordx4 v[196:197], off
	v_lshl_add_u64 v[196:197], v[152:153], 0, s[26:27]
	s_mov_b32 m0, s41
	s_addc_u32 s83, s67, 0
	s_add_i32 s43, s43, s56
	global_load_lds_dwordx4 v[196:197], off
	v_lshl_add_u64 v[196:197], s[82:83], 0, v[140:141]
	s_mov_b32 m0, s43
	s_add_i32 s68, s43, 0x2000
	global_load_lds_dwordx4 v[196:197], off
	v_lshl_add_u64 v[196:197], s[82:83], 0, v[144:145]
	s_mov_b32 m0, s68
	s_nop 0
	global_load_lds_dwordx4 v[196:197], off
	v_lshl_add_u64 v[196:197], v[154:155], 0, s[26:27]
	s_mov_b32 m0, s60
	s_nop 0
	global_load_lds_dwordx4 v[196:197], off
	v_lshl_add_u64 v[196:197], v[156:157], 0, s[26:27]
	s_mov_b32 m0, s61
	s_nop 0
	global_load_lds_dwordx4 v[196:197], off
	s_waitcnt vmcnt(8)
	s_waitcnt lgkmcnt(0)
	s_barrier
	s_setprio 1
	s_waitcnt lgkmcnt(0)
	v_mfma_f32_16x16x128_f8f6f4 v[86:89], v[172:179], v[212:219], v[86:89]
	v_mfma_f32_16x16x128_f8f6f4 v[82:85], v[180:187], v[212:219], v[82:85]
	v_mfma_f32_16x16x128_f8f6f4 v[54:57], v[172:179], v[220:227], v[54:57]
	v_mfma_f32_16x16x128_f8f6f4 v[50:53], v[180:187], v[220:227], v[50:53]
	v_mfma_f32_16x16x128_f8f6f4 v[38:41], v[172:179], v[228:235], v[38:41]
	v_mfma_f32_16x16x128_f8f6f4 v[34:37], v[180:187], v[228:235], v[34:37]
	v_mfma_f32_16x16x128_f8f6f4 v[22:25], v[172:179], v[236:243], v[22:25]
	v_mfma_f32_16x16x128_f8f6f4 v[18:21], v[180:187], v[236:243], v[18:21]
	s_setprio 0
	s_setprio 1
	v_mfma_f32_16x16x128_f8f6f4 v[70:73], v[188:195], v[212:219], v[70:73]
	v_mfma_f32_16x16x128_f8f6f4 v[66:69], v[204:211], v[212:219], v[66:69]
	v_mfma_f32_16x16x128_f8f6f4 v[46:49], v[188:195], v[220:227], v[46:49]
	v_mfma_f32_16x16x128_f8f6f4 v[42:45], v[204:211], v[220:227], v[42:45]
	v_mfma_f32_16x16x128_f8f6f4 v[30:33], v[188:195], v[228:235], v[30:33]
	v_mfma_f32_16x16x128_f8f6f4 v[26:29], v[204:211], v[228:235], v[26:29]
	v_mfma_f32_16x16x128_f8f6f4 v[14:17], v[188:195], v[236:243], v[14:17]
	v_mfma_f32_16x16x128_f8f6f4 v[10:13], v[204:211], v[236:243], v[10:13]
	s_setprio 0
	s_barrier
	ds_read_b128 v[172:175], v162
	ds_read_b128 v[176:179], v162 offset:1024
	ds_read_b128 v[180:183], v162 offset:2048
	ds_read_b128 v[184:187], v162 offset:3072
	ds_read_b128 v[188:191], v163
	ds_read_b128 v[192:195], v163 offset:1024
	ds_read_b128 v[204:207], v163 offset:2048
	ds_read_b128 v[208:211], v163 offset:3072
	s_add_u32 s82, s64, 0x20180
	s_addc_u32 s83, s65, 0
	s_mov_b32 m0, s63
	v_lshl_add_u64 v[196:197], s[82:83], 0, v[138:139]
	ds_read_b128 v[212:215], v161
	ds_read_b128 v[216:219], v161 offset:1024
	ds_read_b128 v[220:223], v161 offset:2048
	ds_read_b128 v[224:227], v161 offset:3072
	ds_read_b128 v[228:231], v161 offset:4096
	ds_read_b128 v[232:235], v161 offset:5120
	ds_read_b128 v[236:239], v161 offset:6144
	ds_read_b128 v[240:243], v161 offset:7168
	global_load_lds_dwordx4 v[196:197], off
	v_lshl_add_u64 v[196:197], s[82:83], 0, v[142:143]
	s_mov_b32 m0, s69
	s_nop 0
	global_load_lds_dwordx4 v[196:197], off
	s_waitcnt vmcnt(8)
	s_waitcnt lgkmcnt(0)
	s_barrier
	s_setprio 1
	s_waitcnt lgkmcnt(0)
	v_mfma_f32_16x16x128_f8f6f4 v[134:137], v[172:179], v[212:219], v[134:137]
	v_mfma_f32_16x16x128_f8f6f4 v[130:133], v[180:187], v[212:219], v[130:133]
	v_mfma_f32_16x16x128_f8f6f4 v[118:121], v[172:179], v[220:227], v[118:121]
	v_mfma_f32_16x16x128_f8f6f4 v[114:117], v[180:187], v[220:227], v[114:117]
	v_mfma_f32_16x16x128_f8f6f4 v[102:105], v[172:179], v[228:235], v[102:105]
	v_mfma_f32_16x16x128_f8f6f4 v[98:101], v[180:187], v[228:235], v[98:101]
	v_mfma_f32_16x16x128_f8f6f4 v[78:81], v[172:179], v[236:243], v[78:81]
	v_mfma_f32_16x16x128_f8f6f4 v[74:77], v[180:187], v[236:243], v[74:77]
	s_setprio 0
	s_setprio 1
	v_mfma_f32_16x16x128_f8f6f4 v[126:129], v[188:195], v[212:219], v[126:129]
	v_mfma_f32_16x16x128_f8f6f4 v[122:125], v[204:211], v[212:219], v[122:125]
	v_mfma_f32_16x16x128_f8f6f4 v[110:113], v[188:195], v[220:227], v[110:113]
	v_mfma_f32_16x16x128_f8f6f4 v[106:109], v[204:211], v[220:227], v[106:109]
	v_mfma_f32_16x16x128_f8f6f4 v[94:97], v[188:195], v[228:235], v[94:97]
	v_mfma_f32_16x16x128_f8f6f4 v[90:93], v[204:211], v[228:235], v[90:93]
	v_mfma_f32_16x16x128_f8f6f4 v[62:65], v[188:195], v[236:243], v[62:65]
	v_mfma_f32_16x16x128_f8f6f4 v[58:61], v[204:211], v[236:243], v[58:61]
	s_setprio 0
	s_barrier
	s_mov_b32 m0, s80
	v_lshl_add_u64 v[196:197], v[150:151], 0, s[28:29]
	s_add_u32 s82, s66, 0x8200
	ds_read_b128 v[212:215], v161 offset:16384
	ds_read_b128 v[216:219], v161 offset:17408
	ds_read_b128 v[220:223], v161 offset:18432
	ds_read_b128 v[224:227], v161 offset:19456
	ds_read_b128 v[228:231], v161 offset:20480
	ds_read_b128 v[232:235], v161 offset:21504
	ds_read_b128 v[236:239], v161 offset:22528
	ds_read_b128 v[240:243], v161 offset:23552
	global_load_lds_dwordx4 v[196:197], off
	v_lshl_add_u64 v[196:197], v[152:153], 0, s[28:29]
	s_mov_b32 m0, s76
	s_addc_u32 s83, s67, 0
	global_load_lds_dwordx4 v[196:197], off
	v_lshl_add_u64 v[196:197], s[82:83], 0, v[140:141]
	s_mov_b32 m0, s77
	s_nop 0
	global_load_lds_dwordx4 v[196:197], off
	v_lshl_add_u64 v[196:197], s[82:83], 0, v[144:145]
	s_mov_b32 m0, s78
	s_nop 0
	global_load_lds_dwordx4 v[196:197], off
	v_lshl_add_u64 v[196:197], v[154:155], 0, s[28:29]
	s_mov_b32 m0, s51
	s_nop 0
	global_load_lds_dwordx4 v[196:197], off
	v_lshl_add_u64 v[196:197], v[156:157], 0, s[28:29]
	s_mov_b32 m0, s57
	s_nop 0
	global_load_lds_dwordx4 v[196:197], off
	s_waitcnt vmcnt(8)
	s_waitcnt lgkmcnt(0)
	s_barrier
	s_setprio 1
	s_waitcnt lgkmcnt(0)
	v_mfma_f32_16x16x128_f8f6f4 v[86:89], v[172:179], v[212:219], v[86:89]
	v_mfma_f32_16x16x128_f8f6f4 v[82:85], v[180:187], v[212:219], v[82:85]
	v_mfma_f32_16x16x128_f8f6f4 v[54:57], v[172:179], v[220:227], v[54:57]
	v_mfma_f32_16x16x128_f8f6f4 v[50:53], v[180:187], v[220:227], v[50:53]
	v_mfma_f32_16x16x128_f8f6f4 v[38:41], v[172:179], v[228:235], v[38:41]
	v_mfma_f32_16x16x128_f8f6f4 v[34:37], v[180:187], v[228:235], v[34:37]
	v_mfma_f32_16x16x128_f8f6f4 v[22:25], v[172:179], v[236:243], v[22:25]
	v_mfma_f32_16x16x128_f8f6f4 v[18:21], v[180:187], v[236:243], v[18:21]
	s_setprio 0
	s_setprio 1
	v_mfma_f32_16x16x128_f8f6f4 v[70:73], v[188:195], v[212:219], v[70:73]
	v_mfma_f32_16x16x128_f8f6f4 v[66:69], v[204:211], v[212:219], v[66:69]
	v_mfma_f32_16x16x128_f8f6f4 v[46:49], v[188:195], v[220:227], v[46:49]
	v_mfma_f32_16x16x128_f8f6f4 v[42:45], v[204:211], v[220:227], v[42:45]
	v_mfma_f32_16x16x128_f8f6f4 v[30:33], v[188:195], v[228:235], v[30:33]
	v_mfma_f32_16x16x128_f8f6f4 v[26:29], v[204:211], v[228:235], v[26:29]
	v_mfma_f32_16x16x128_f8f6f4 v[14:17], v[188:195], v[236:243], v[14:17]
	v_mfma_f32_16x16x128_f8f6f4 v[10:13], v[204:211], v[236:243], v[10:13]
	s_setprio 0
	s_barrier
	ds_read_b128 v[172:175], v158
	ds_read_b128 v[176:179], v158 offset:1024
	ds_read_b128 v[180:183], v158 offset:2048
	ds_read_b128 v[184:187], v158 offset:3072
	ds_read_b128 v[188:191], v159
	ds_read_b128 v[192:195], v159 offset:1024
	ds_read_b128 v[204:207], v159 offset:2048
	ds_read_b128 v[208:211], v159 offset:3072
	s_add_u32 s82, s64, 0x20200
	s_addc_u32 s83, s65, 0
	s_mov_b32 m0, s58
	v_lshl_add_u64 v[196:197], s[82:83], 0, v[138:139]
	ds_read_b128 v[212:215], v161 offset:32768
	ds_read_b128 v[216:219], v161 offset:33792
	ds_read_b128 v[220:223], v161 offset:34816
	ds_read_b128 v[224:227], v161 offset:35840
	ds_read_b128 v[228:231], v161 offset:36864
	ds_read_b128 v[232:235], v161 offset:37888
	ds_read_b128 v[236:239], v161 offset:38912
	ds_read_b128 v[240:243], v161 offset:39936
	global_load_lds_dwordx4 v[196:197], off
	v_lshl_add_u64 v[196:197], s[82:83], 0, v[142:143]
	s_mov_b32 m0, s59
	s_nop 0
	global_load_lds_dwordx4 v[196:197], off
	s_waitcnt vmcnt(8)
	s_waitcnt lgkmcnt(0)
	s_barrier
	s_setprio 1
	s_waitcnt lgkmcnt(0)
	v_mfma_f32_16x16x128_f8f6f4 v[134:137], v[172:179], v[212:219], v[134:137]
	v_mfma_f32_16x16x128_f8f6f4 v[130:133], v[180:187], v[212:219], v[130:133]
	v_mfma_f32_16x16x128_f8f6f4 v[118:121], v[172:179], v[220:227], v[118:121]
	v_mfma_f32_16x16x128_f8f6f4 v[114:117], v[180:187], v[220:227], v[114:117]
	v_mfma_f32_16x16x128_f8f6f4 v[102:105], v[172:179], v[228:235], v[102:105]
	v_mfma_f32_16x16x128_f8f6f4 v[98:101], v[180:187], v[228:235], v[98:101]
	v_mfma_f32_16x16x128_f8f6f4 v[78:81], v[172:179], v[236:243], v[78:81]
	v_mfma_f32_16x16x128_f8f6f4 v[74:77], v[180:187], v[236:243], v[74:77]
	s_setprio 0
	s_setprio 1
	v_mfma_f32_16x16x128_f8f6f4 v[126:129], v[188:195], v[212:219], v[126:129]
	v_mfma_f32_16x16x128_f8f6f4 v[122:125], v[204:211], v[212:219], v[122:125]
	v_mfma_f32_16x16x128_f8f6f4 v[110:113], v[188:195], v[220:227], v[110:113]
	v_mfma_f32_16x16x128_f8f6f4 v[106:109], v[204:211], v[220:227], v[106:109]
	v_mfma_f32_16x16x128_f8f6f4 v[94:97], v[188:195], v[228:235], v[94:97]
	v_mfma_f32_16x16x128_f8f6f4 v[90:93], v[204:211], v[228:235], v[90:93]
	v_mfma_f32_16x16x128_f8f6f4 v[62:65], v[188:195], v[236:243], v[62:65]
	v_mfma_f32_16x16x128_f8f6f4 v[58:61], v[204:211], v[236:243], v[58:61]
	s_setprio 0
	s_barrier
	s_mov_b32 m0, s79
	v_lshl_add_u64 v[196:197], v[150:151], 0, s[30:31]
	s_add_u32 s82, s66, 0x8280
	ds_read_b128 v[212:215], v161 offset:49152
	ds_read_b128 v[216:219], v161 offset:50176
	ds_read_b128 v[220:223], v161 offset:51200
	ds_read_b128 v[224:227], v161 offset:52224
	ds_read_b128 v[228:231], v161 offset:53248
	ds_read_b128 v[232:235], v161 offset:54272
	ds_read_b128 v[236:239], v161 offset:55296
	ds_read_b128 v[240:243], v161 offset:56320
	global_load_lds_dwordx4 v[196:197], off
	v_lshl_add_u64 v[196:197], v[152:153], 0, s[30:31]
	s_mov_b32 m0, s41
	s_addc_u32 s83, s67, 0
	global_load_lds_dwordx4 v[196:197], off
	v_lshl_add_u64 v[196:197], s[82:83], 0, v[140:141]
	s_mov_b32 m0, s43
	s_nop 0
	global_load_lds_dwordx4 v[196:197], off
	v_lshl_add_u64 v[196:197], s[82:83], 0, v[144:145]
	s_mov_b32 m0, s68
	s_nop 0
	global_load_lds_dwordx4 v[196:197], off
	v_lshl_add_u64 v[196:197], v[154:155], 0, s[30:31]
	s_mov_b32 m0, s60
	s_nop 0
	global_load_lds_dwordx4 v[196:197], off
	v_lshl_add_u64 v[196:197], v[156:157], 0, s[30:31]
	s_mov_b32 m0, s61
	s_nop 0
	global_load_lds_dwordx4 v[196:197], off
	s_waitcnt vmcnt(8)
	s_waitcnt lgkmcnt(0)
	s_barrier
	s_setprio 1
	s_waitcnt lgkmcnt(0)
	v_mfma_f32_16x16x128_f8f6f4 v[86:89], v[172:179], v[212:219], v[86:89]
	v_mfma_f32_16x16x128_f8f6f4 v[82:85], v[180:187], v[212:219], v[82:85]
	v_mfma_f32_16x16x128_f8f6f4 v[54:57], v[172:179], v[220:227], v[54:57]
	v_mfma_f32_16x16x128_f8f6f4 v[50:53], v[180:187], v[220:227], v[50:53]
	v_mfma_f32_16x16x128_f8f6f4 v[38:41], v[172:179], v[228:235], v[38:41]
	v_mfma_f32_16x16x128_f8f6f4 v[34:37], v[180:187], v[228:235], v[34:37]
	v_mfma_f32_16x16x128_f8f6f4 v[22:25], v[172:179], v[236:243], v[22:25]
	v_mfma_f32_16x16x128_f8f6f4 v[18:21], v[180:187], v[236:243], v[18:21]
	s_setprio 0
	s_setprio 1
	v_mfma_f32_16x16x128_f8f6f4 v[70:73], v[188:195], v[212:219], v[70:73]
	v_mfma_f32_16x16x128_f8f6f4 v[66:69], v[204:211], v[212:219], v[66:69]
	v_mfma_f32_16x16x128_f8f6f4 v[46:49], v[188:195], v[220:227], v[46:49]
	v_mfma_f32_16x16x128_f8f6f4 v[42:45], v[204:211], v[220:227], v[42:45]
	v_mfma_f32_16x16x128_f8f6f4 v[30:33], v[188:195], v[228:235], v[30:33]
	v_mfma_f32_16x16x128_f8f6f4 v[26:29], v[204:211], v[228:235], v[26:29]
	v_mfma_f32_16x16x128_f8f6f4 v[14:17], v[188:195], v[236:243], v[14:17]
	v_mfma_f32_16x16x128_f8f6f4 v[10:13], v[204:211], v[236:243], v[10:13]
	s_setprio 0
	s_barrier
	ds_read_b128 v[172:175], v162
	ds_read_b128 v[176:179], v162 offset:1024
	ds_read_b128 v[180:183], v162 offset:2048
	ds_read_b128 v[184:187], v162 offset:3072
	ds_read_b128 v[188:191], v163
	ds_read_b128 v[192:195], v163 offset:1024
	ds_read_b128 v[204:207], v163 offset:2048
	ds_read_b128 v[208:211], v163 offset:3072
	s_add_u32 s82, s64, 0x20280
	s_addc_u32 s83, s65, 0
	s_mov_b32 m0, s63
	v_lshl_add_u64 v[196:197], s[82:83], 0, v[138:139]
	ds_read_b128 v[212:215], v161
	ds_read_b128 v[216:219], v161 offset:1024
	ds_read_b128 v[220:223], v161 offset:2048
	ds_read_b128 v[224:227], v161 offset:3072
	ds_read_b128 v[228:231], v161 offset:4096
	ds_read_b128 v[232:235], v161 offset:5120
	ds_read_b128 v[236:239], v161 offset:6144
	ds_read_b128 v[240:243], v161 offset:7168
	global_load_lds_dwordx4 v[196:197], off
	v_lshl_add_u64 v[196:197], s[82:83], 0, v[142:143]
	s_mov_b32 m0, s69
	s_nop 0
	global_load_lds_dwordx4 v[196:197], off
	s_waitcnt vmcnt(8)
	s_waitcnt lgkmcnt(0)
	s_barrier
	s_setprio 1
	s_waitcnt lgkmcnt(0)
	v_mfma_f32_16x16x128_f8f6f4 v[134:137], v[172:179], v[212:219], v[134:137]
	v_mfma_f32_16x16x128_f8f6f4 v[130:133], v[180:187], v[212:219], v[130:133]
	v_mfma_f32_16x16x128_f8f6f4 v[118:121], v[172:179], v[220:227], v[118:121]
	v_mfma_f32_16x16x128_f8f6f4 v[114:117], v[180:187], v[220:227], v[114:117]
	v_mfma_f32_16x16x128_f8f6f4 v[102:105], v[172:179], v[228:235], v[102:105]
	v_mfma_f32_16x16x128_f8f6f4 v[98:101], v[180:187], v[228:235], v[98:101]
	v_mfma_f32_16x16x128_f8f6f4 v[78:81], v[172:179], v[236:243], v[78:81]
	v_mfma_f32_16x16x128_f8f6f4 v[74:77], v[180:187], v[236:243], v[74:77]
	s_setprio 0
	s_setprio 1
	v_mfma_f32_16x16x128_f8f6f4 v[126:129], v[188:195], v[212:219], v[126:129]
	v_mfma_f32_16x16x128_f8f6f4 v[122:125], v[204:211], v[212:219], v[122:125]
	v_mfma_f32_16x16x128_f8f6f4 v[110:113], v[188:195], v[220:227], v[110:113]
	v_mfma_f32_16x16x128_f8f6f4 v[106:109], v[204:211], v[220:227], v[106:109]
	v_mfma_f32_16x16x128_f8f6f4 v[94:97], v[188:195], v[228:235], v[94:97]
	v_mfma_f32_16x16x128_f8f6f4 v[90:93], v[204:211], v[228:235], v[90:93]
	v_mfma_f32_16x16x128_f8f6f4 v[62:65], v[188:195], v[236:243], v[62:65]
	v_mfma_f32_16x16x128_f8f6f4 v[58:61], v[204:211], v[236:243], v[58:61]
	s_setprio 0
	s_barrier
	s_mov_b32 m0, s80
	v_lshl_add_u64 v[196:197], v[150:151], 0, s[34:35]
	s_add_u32 s82, s66, 0x8300
	ds_read_b128 v[212:215], v161 offset:16384
	ds_read_b128 v[216:219], v161 offset:17408
	ds_read_b128 v[220:223], v161 offset:18432
	ds_read_b128 v[224:227], v161 offset:19456
	ds_read_b128 v[228:231], v161 offset:20480
	ds_read_b128 v[232:235], v161 offset:21504
	ds_read_b128 v[236:239], v161 offset:22528
	ds_read_b128 v[240:243], v161 offset:23552
	global_load_lds_dwordx4 v[196:197], off
	v_lshl_add_u64 v[196:197], v[152:153], 0, s[34:35]
	s_mov_b32 m0, s76
	s_addc_u32 s83, s67, 0
	global_load_lds_dwordx4 v[196:197], off
	v_lshl_add_u64 v[196:197], s[82:83], 0, v[140:141]
	s_mov_b32 m0, s77
	s_nop 0
	global_load_lds_dwordx4 v[196:197], off
	v_lshl_add_u64 v[196:197], s[82:83], 0, v[144:145]
	s_mov_b32 m0, s78
	s_nop 0
	global_load_lds_dwordx4 v[196:197], off
	v_lshl_add_u64 v[196:197], v[154:155], 0, s[34:35]
	s_mov_b32 m0, s51
	s_nop 0
	global_load_lds_dwordx4 v[196:197], off
	v_lshl_add_u64 v[196:197], v[156:157], 0, s[34:35]
	s_mov_b32 m0, s57
	s_nop 0
	global_load_lds_dwordx4 v[196:197], off
	s_waitcnt vmcnt(8)
	s_waitcnt lgkmcnt(0)
	s_barrier
	s_setprio 1
	s_waitcnt lgkmcnt(0)
	v_mfma_f32_16x16x128_f8f6f4 v[86:89], v[172:179], v[212:219], v[86:89]
	v_mfma_f32_16x16x128_f8f6f4 v[82:85], v[180:187], v[212:219], v[82:85]
	v_mfma_f32_16x16x128_f8f6f4 v[54:57], v[172:179], v[220:227], v[54:57]
	v_mfma_f32_16x16x128_f8f6f4 v[50:53], v[180:187], v[220:227], v[50:53]
	v_mfma_f32_16x16x128_f8f6f4 v[38:41], v[172:179], v[228:235], v[38:41]
	v_mfma_f32_16x16x128_f8f6f4 v[34:37], v[180:187], v[228:235], v[34:37]
	v_mfma_f32_16x16x128_f8f6f4 v[22:25], v[172:179], v[236:243], v[22:25]
	v_mfma_f32_16x16x128_f8f6f4 v[18:21], v[180:187], v[236:243], v[18:21]
	s_setprio 0
	s_setprio 1
	v_mfma_f32_16x16x128_f8f6f4 v[70:73], v[188:195], v[212:219], v[70:73]
	v_mfma_f32_16x16x128_f8f6f4 v[66:69], v[204:211], v[212:219], v[66:69]
	v_mfma_f32_16x16x128_f8f6f4 v[46:49], v[188:195], v[220:227], v[46:49]
	v_mfma_f32_16x16x128_f8f6f4 v[42:45], v[204:211], v[220:227], v[42:45]
	v_mfma_f32_16x16x128_f8f6f4 v[30:33], v[188:195], v[228:235], v[30:33]
	v_mfma_f32_16x16x128_f8f6f4 v[26:29], v[204:211], v[228:235], v[26:29]
	v_mfma_f32_16x16x128_f8f6f4 v[14:17], v[188:195], v[236:243], v[14:17]
	v_mfma_f32_16x16x128_f8f6f4 v[10:13], v[204:211], v[236:243], v[10:13]
	s_setprio 0
	s_barrier
	ds_read_b128 v[172:175], v158
	ds_read_b128 v[176:179], v158 offset:1024
	ds_read_b128 v[180:183], v158 offset:2048
	ds_read_b128 v[184:187], v158 offset:3072
	ds_read_b128 v[188:191], v159
	ds_read_b128 v[192:195], v159 offset:1024
	ds_read_b128 v[204:207], v159 offset:2048
	ds_read_b128 v[208:211], v159 offset:3072
	s_add_u32 s82, s64, 0x20300
	s_addc_u32 s83, s65, 0
	s_mov_b32 m0, s58
	v_lshl_add_u64 v[196:197], s[82:83], 0, v[138:139]
	ds_read_b128 v[212:215], v161 offset:32768
	ds_read_b128 v[216:219], v161 offset:33792
	ds_read_b128 v[220:223], v161 offset:34816
	ds_read_b128 v[224:227], v161 offset:35840
	ds_read_b128 v[228:231], v161 offset:36864
	ds_read_b128 v[232:235], v161 offset:37888
	ds_read_b128 v[236:239], v161 offset:38912
	ds_read_b128 v[240:243], v161 offset:39936
	global_load_lds_dwordx4 v[196:197], off
	v_lshl_add_u64 v[196:197], s[82:83], 0, v[142:143]
	s_mov_b32 m0, s59
	s_nop 0
	global_load_lds_dwordx4 v[196:197], off
	s_waitcnt vmcnt(8)
	s_waitcnt lgkmcnt(0)
	s_barrier
	s_setprio 1
	s_waitcnt lgkmcnt(0)
	v_mfma_f32_16x16x128_f8f6f4 v[134:137], v[172:179], v[212:219], v[134:137]
	v_mfma_f32_16x16x128_f8f6f4 v[130:133], v[180:187], v[212:219], v[130:133]
	v_mfma_f32_16x16x128_f8f6f4 v[118:121], v[172:179], v[220:227], v[118:121]
	v_mfma_f32_16x16x128_f8f6f4 v[114:117], v[180:187], v[220:227], v[114:117]
	v_mfma_f32_16x16x128_f8f6f4 v[102:105], v[172:179], v[228:235], v[102:105]
	v_mfma_f32_16x16x128_f8f6f4 v[98:101], v[180:187], v[228:235], v[98:101]
	v_mfma_f32_16x16x128_f8f6f4 v[78:81], v[172:179], v[236:243], v[78:81]
	v_mfma_f32_16x16x128_f8f6f4 v[74:77], v[180:187], v[236:243], v[74:77]
	s_setprio 0
	s_setprio 1
	v_mfma_f32_16x16x128_f8f6f4 v[126:129], v[188:195], v[212:219], v[126:129]
	v_mfma_f32_16x16x128_f8f6f4 v[122:125], v[204:211], v[212:219], v[122:125]
	v_mfma_f32_16x16x128_f8f6f4 v[110:113], v[188:195], v[220:227], v[110:113]
	v_mfma_f32_16x16x128_f8f6f4 v[106:109], v[204:211], v[220:227], v[106:109]
	v_mfma_f32_16x16x128_f8f6f4 v[94:97], v[188:195], v[228:235], v[94:97]
	v_mfma_f32_16x16x128_f8f6f4 v[90:93], v[204:211], v[228:235], v[90:93]
	v_mfma_f32_16x16x128_f8f6f4 v[62:65], v[188:195], v[236:243], v[62:65]
	v_mfma_f32_16x16x128_f8f6f4 v[58:61], v[204:211], v[236:243], v[58:61]
	s_setprio 0
	s_barrier
	s_mov_b32 m0, s79
	v_lshl_add_u64 v[150:151], v[150:151], 0, s[36:37]
	s_add_u32 s66, s66, 0x8380
	ds_read_b128 v[212:215], v161 offset:49152
	ds_read_b128 v[216:219], v161 offset:50176
	ds_read_b128 v[220:223], v161 offset:51200
	ds_read_b128 v[224:227], v161 offset:52224
	ds_read_b128 v[228:231], v161 offset:53248
	ds_read_b128 v[232:235], v161 offset:54272
	ds_read_b128 v[236:239], v161 offset:55296
	ds_read_b128 v[240:243], v161 offset:56320
	global_load_lds_dwordx4 v[150:151], off
	v_lshl_add_u64 v[150:151], v[152:153], 0, s[36:37]
	s_mov_b32 m0, s41
	s_addc_u32 s67, s67, 0
	global_load_lds_dwordx4 v[150:151], off
	v_lshl_add_u64 v[150:151], s[66:67], 0, v[140:141]
	s_mov_b32 m0, s43
	s_nop 0
	global_load_lds_dwordx4 v[150:151], off
	v_lshl_add_u64 v[150:151], s[66:67], 0, v[144:145]
	s_mov_b32 m0, s68
	s_nop 0
	global_load_lds_dwordx4 v[150:151], off
	v_lshl_add_u64 v[150:151], v[154:155], 0, s[36:37]
	s_mov_b32 m0, s60
	s_nop 0
	global_load_lds_dwordx4 v[150:151], off
	v_lshl_add_u64 v[150:151], v[156:157], 0, s[36:37]
	s_mov_b32 m0, s61
	s_nop 0
	global_load_lds_dwordx4 v[150:151], off
	s_waitcnt vmcnt(8)
	s_waitcnt lgkmcnt(0)
	s_barrier
	s_setprio 1
	s_waitcnt lgkmcnt(0)
	v_mfma_f32_16x16x128_f8f6f4 v[86:89], v[172:179], v[212:219], v[86:89]
	v_mfma_f32_16x16x128_f8f6f4 v[82:85], v[180:187], v[212:219], v[82:85]
	v_mfma_f32_16x16x128_f8f6f4 v[54:57], v[172:179], v[220:227], v[54:57]
	v_mfma_f32_16x16x128_f8f6f4 v[50:53], v[180:187], v[220:227], v[50:53]
	v_mfma_f32_16x16x128_f8f6f4 v[38:41], v[172:179], v[228:235], v[38:41]
	v_mfma_f32_16x16x128_f8f6f4 v[34:37], v[180:187], v[228:235], v[34:37]
	v_mfma_f32_16x16x128_f8f6f4 v[22:25], v[172:179], v[236:243], v[22:25]
	v_mfma_f32_16x16x128_f8f6f4 v[18:21], v[180:187], v[236:243], v[18:21]
	s_setprio 0
	s_setprio 1
	v_mfma_f32_16x16x128_f8f6f4 v[70:73], v[188:195], v[212:219], v[70:73]
	v_mfma_f32_16x16x128_f8f6f4 v[66:69], v[204:211], v[212:219], v[66:69]
	v_mfma_f32_16x16x128_f8f6f4 v[46:49], v[188:195], v[220:227], v[46:49]
	v_mfma_f32_16x16x128_f8f6f4 v[42:45], v[204:211], v[220:227], v[42:45]
	v_mfma_f32_16x16x128_f8f6f4 v[30:33], v[188:195], v[228:235], v[30:33]
	v_mfma_f32_16x16x128_f8f6f4 v[26:29], v[204:211], v[228:235], v[26:29]
	v_mfma_f32_16x16x128_f8f6f4 v[14:17], v[188:195], v[236:243], v[14:17]
	v_mfma_f32_16x16x128_f8f6f4 v[10:13], v[204:211], v[236:243], v[10:13]
	s_setprio 0
	s_barrier
	ds_read_b128 v[150:153], v162
	ds_read_b128 v[154:157], v162 offset:1024
	ds_read_b128 v[172:175], v162 offset:2048
	ds_read_b128 v[176:179], v162 offset:3072
	ds_read_b128 v[180:183], v163
	ds_read_b128 v[184:187], v163 offset:1024
	ds_read_b128 v[188:191], v163 offset:2048
	ds_read_b128 v[192:195], v163 offset:3072
	s_add_u32 s64, s64, 0x20380
	s_addc_u32 s65, s65, 0
	s_mov_b32 m0, s63
	v_lshl_add_u64 v[196:197], s[64:65], 0, v[138:139]
	ds_read_b128 v[204:207], v161
	ds_read_b128 v[208:211], v161 offset:1024
	ds_read_b128 v[212:215], v161 offset:2048
	ds_read_b128 v[216:219], v161 offset:3072
	ds_read_b128 v[220:223], v161 offset:4096
	ds_read_b128 v[224:227], v161 offset:5120
	ds_read_b128 v[228:231], v161 offset:6144
	ds_read_b128 v[232:235], v161 offset:7168
	global_load_lds_dwordx4 v[196:197], off
	v_lshl_add_u64 v[196:197], s[64:65], 0, v[142:143]
	s_mov_b32 m0, s69
	s_nop 0
	global_load_lds_dwordx4 v[196:197], off
	s_waitcnt vmcnt(8)
	s_waitcnt lgkmcnt(0)
	s_barrier
	s_setprio 1
	s_waitcnt lgkmcnt(0)
	v_mfma_f32_16x16x128_f8f6f4 v[134:137], v[150:157], v[204:211], v[134:137]
	v_mfma_f32_16x16x128_f8f6f4 v[130:133], v[172:179], v[204:211], v[130:133]
	v_mfma_f32_16x16x128_f8f6f4 v[118:121], v[150:157], v[212:219], v[118:121]
	v_mfma_f32_16x16x128_f8f6f4 v[114:117], v[172:179], v[212:219], v[114:117]
	v_mfma_f32_16x16x128_f8f6f4 v[102:105], v[150:157], v[220:227], v[102:105]
	v_mfma_f32_16x16x128_f8f6f4 v[98:101], v[172:179], v[220:227], v[98:101]
	v_mfma_f32_16x16x128_f8f6f4 v[78:81], v[150:157], v[228:235], v[78:81]
	v_mfma_f32_16x16x128_f8f6f4 v[74:77], v[172:179], v[228:235], v[74:77]
	s_setprio 0
	s_setprio 1
	v_mfma_f32_16x16x128_f8f6f4 v[126:129], v[180:187], v[204:211], v[126:129]
	v_mfma_f32_16x16x128_f8f6f4 v[122:125], v[188:195], v[204:211], v[122:125]
	v_mfma_f32_16x16x128_f8f6f4 v[110:113], v[180:187], v[212:219], v[110:113]
	v_mfma_f32_16x16x128_f8f6f4 v[106:109], v[188:195], v[212:219], v[106:109]
	v_mfma_f32_16x16x128_f8f6f4 v[94:97], v[180:187], v[220:227], v[94:97]
	v_mfma_f32_16x16x128_f8f6f4 v[90:93], v[188:195], v[220:227], v[90:93]
	v_mfma_f32_16x16x128_f8f6f4 v[62:65], v[180:187], v[228:235], v[62:65]
	v_mfma_f32_16x16x128_f8f6f4 v[58:61], v[188:195], v[228:235], v[58:61]
	s_setprio 0
	s_barrier
	s_mov_b32 m0, s80
	v_lshl_add_u64 v[196:197], s[10:11], 0, v[140:141]
	s_add_u32 s64, s10, 0x8000
	ds_read_b128 v[204:207], v161 offset:16384
	ds_read_b128 v[208:211], v161 offset:17408
	ds_read_b128 v[212:215], v161 offset:18432
	ds_read_b128 v[216:219], v161 offset:19456
	ds_read_b128 v[220:223], v161 offset:20480
	ds_read_b128 v[224:227], v161 offset:21504
	ds_read_b128 v[228:231], v161 offset:22528
	ds_read_b128 v[232:235], v161 offset:23552
	global_load_lds_dwordx4 v[196:197], off
	v_lshl_add_u64 v[198:199], s[10:11], 0, v[144:145]
	s_mov_b32 m0, s76
	s_addc_u32 s65, s11, 0
	global_load_lds_dwordx4 v[198:199], off
	v_lshl_add_u64 v[200:201], s[64:65], 0, v[140:141]
	s_mov_b32 m0, s77
	v_lshl_add_u64 v[236:237], s[70:71], 0, v[142:143]
	global_load_lds_dwordx4 v[200:201], off
	v_lshl_add_u64 v[200:201], s[64:65], 0, v[144:145]
	s_mov_b32 m0, s78
	s_nop 0
	global_load_lds_dwordx4 v[200:201], off
	v_lshl_add_u64 v[200:201], s[70:71], 0, v[138:139]
	s_mov_b32 m0, s51
	s_nop 0
	global_load_lds_dwordx4 v[200:201], off
	s_mov_b32 m0, s57
	s_nop 0
	global_load_lds_dwordx4 v[236:237], off
	s_waitcnt vmcnt(8)
	s_waitcnt lgkmcnt(0)
	s_barrier
	s_setprio 1
	s_waitcnt lgkmcnt(0)
	v_mfma_f32_16x16x128_f8f6f4 v[86:89], v[150:157], v[204:211], v[86:89]
	v_mfma_f32_16x16x128_f8f6f4 v[82:85], v[172:179], v[204:211], v[82:85]
	v_mfma_f32_16x16x128_f8f6f4 v[54:57], v[150:157], v[212:219], v[54:57]
	v_mfma_f32_16x16x128_f8f6f4 v[50:53], v[172:179], v[212:219], v[50:53]
	v_mfma_f32_16x16x128_f8f6f4 v[38:41], v[150:157], v[220:227], v[38:41]
	v_mfma_f32_16x16x128_f8f6f4 v[34:37], v[172:179], v[220:227], v[34:37]
	v_mfma_f32_16x16x128_f8f6f4 v[22:25], v[150:157], v[228:235], v[22:25]
	v_mfma_f32_16x16x128_f8f6f4 v[18:21], v[172:179], v[228:235], v[18:21]
	s_setprio 0
	s_setprio 1
	v_mfma_f32_16x16x128_f8f6f4 v[70:73], v[180:187], v[204:211], v[70:73]
	v_mfma_f32_16x16x128_f8f6f4 v[66:69], v[188:195], v[204:211], v[66:69]
	v_mfma_f32_16x16x128_f8f6f4 v[46:49], v[180:187], v[212:219], v[46:49]
	v_mfma_f32_16x16x128_f8f6f4 v[42:45], v[188:195], v[212:219], v[42:45]
	v_mfma_f32_16x16x128_f8f6f4 v[30:33], v[180:187], v[220:227], v[30:33]
	v_mfma_f32_16x16x128_f8f6f4 v[26:29], v[188:195], v[220:227], v[26:29]
	v_mfma_f32_16x16x128_f8f6f4 v[14:17], v[180:187], v[228:235], v[14:17]
	v_mfma_f32_16x16x128_f8f6f4 v[10:13], v[188:195], v[228:235], v[10:13]
	s_setprio 0
	s_barrier
	ds_read_b128 v[150:153], v158
	ds_read_b128 v[154:157], v158 offset:1024
	ds_read_b128 v[172:175], v158 offset:2048
	ds_read_b128 v[176:179], v158 offset:3072
	ds_read_b128 v[180:183], v159
	ds_read_b128 v[184:187], v159 offset:1024
	ds_read_b128 v[188:191], v159 offset:2048
	ds_read_b128 v[192:195], v159 offset:3072
	s_add_u32 s64, s70, 0x20000
	s_addc_u32 s65, s71, 0
	s_mov_b32 m0, s58
	v_lshl_add_u64 v[158:159], s[64:65], 0, v[138:139]
	ds_read_b128 v[204:207], v161 offset:32768
	ds_read_b128 v[208:211], v161 offset:33792
	ds_read_b128 v[212:215], v161 offset:34816
	ds_read_b128 v[216:219], v161 offset:35840
	ds_read_b128 v[220:223], v161 offset:36864
	ds_read_b128 v[224:227], v161 offset:37888
	ds_read_b128 v[228:231], v161 offset:38912
	ds_read_b128 v[232:235], v161 offset:39936
	global_load_lds_dwordx4 v[158:159], off
	v_lshl_add_u64 v[158:159], s[64:65], 0, v[142:143]
	s_mov_b32 m0, s59
	s_nop 0
	global_load_lds_dwordx4 v[158:159], off
	s_waitcnt vmcnt(8)
	s_waitcnt lgkmcnt(0)
	s_barrier
	s_setprio 1
	s_waitcnt lgkmcnt(0)
	v_mfma_f32_16x16x128_f8f6f4 v[134:137], v[150:157], v[204:211], v[134:137]
	v_mfma_f32_16x16x128_f8f6f4 v[130:133], v[172:179], v[204:211], v[130:133]
	v_mfma_f32_16x16x128_f8f6f4 v[118:121], v[150:157], v[212:219], v[118:121]
	v_mfma_f32_16x16x128_f8f6f4 v[114:117], v[172:179], v[212:219], v[114:117]
	v_mfma_f32_16x16x128_f8f6f4 v[102:105], v[150:157], v[220:227], v[102:105]
	v_mfma_f32_16x16x128_f8f6f4 v[98:101], v[172:179], v[220:227], v[98:101]
	v_mfma_f32_16x16x128_f8f6f4 v[78:81], v[150:157], v[228:235], v[78:81]
	v_mfma_f32_16x16x128_f8f6f4 v[74:77], v[172:179], v[228:235], v[74:77]
	s_setprio 0
	s_setprio 1
	v_mfma_f32_16x16x128_f8f6f4 v[126:129], v[180:187], v[204:211], v[126:129]
	v_mfma_f32_16x16x128_f8f6f4 v[122:125], v[188:195], v[204:211], v[122:125]
	v_mfma_f32_16x16x128_f8f6f4 v[110:113], v[180:187], v[212:219], v[110:113]
	v_mfma_f32_16x16x128_f8f6f4 v[106:109], v[188:195], v[212:219], v[106:109]
	v_mfma_f32_16x16x128_f8f6f4 v[94:97], v[180:187], v[220:227], v[94:97]
	v_mfma_f32_16x16x128_f8f6f4 v[90:93], v[188:195], v[220:227], v[90:93]
	v_mfma_f32_16x16x128_f8f6f4 v[62:65], v[180:187], v[228:235], v[62:65]
	v_mfma_f32_16x16x128_f8f6f4 v[58:61], v[188:195], v[228:235], v[58:61]
	s_setprio 0
	s_barrier
	s_mov_b32 m0, s79
	v_lshl_add_u64 v[158:159], v[196:197], 0, s[18:19]
	s_add_u32 s10, s10, 0x8080
	ds_read_b128 v[204:207], v161 offset:49152
	ds_read_b128 v[208:211], v161 offset:50176
	ds_read_b128 v[212:215], v161 offset:51200
	ds_read_b128 v[216:219], v161 offset:52224
	ds_read_b128 v[220:223], v161 offset:53248
	ds_read_b128 v[224:227], v161 offset:54272
	ds_read_b128 v[228:231], v161 offset:55296
	ds_read_b128 v[232:235], v161 offset:56320
	global_load_lds_dwordx4 v[158:159], off
	v_lshl_add_u64 v[158:159], v[198:199], 0, s[18:19]
	s_mov_b32 m0, s41
	s_addc_u32 s11, s11, 0
	global_load_lds_dwordx4 v[158:159], off
	v_lshl_add_u64 v[158:159], s[10:11], 0, v[140:141]
	s_mov_b32 m0, s43
	s_nop 0
	global_load_lds_dwordx4 v[158:159], off
	v_lshl_add_u64 v[158:159], s[10:11], 0, v[144:145]
	s_mov_b32 m0, s68
	s_nop 0
	global_load_lds_dwordx4 v[158:159], off
	v_lshl_add_u64 v[158:159], v[200:201], 0, s[18:19]
	s_mov_b32 m0, s60
	s_nop 0
	global_load_lds_dwordx4 v[158:159], off
	v_lshl_add_u64 v[158:159], v[236:237], 0, s[18:19]
	s_mov_b32 m0, s61
	s_nop 0
	global_load_lds_dwordx4 v[158:159], off
	s_waitcnt vmcnt(8)
	s_waitcnt lgkmcnt(0)
	s_barrier
	s_setprio 1
	s_waitcnt lgkmcnt(0)
	v_mfma_f32_16x16x128_f8f6f4 v[86:89], v[150:157], v[204:211], v[86:89]
	v_mfma_f32_16x16x128_f8f6f4 v[82:85], v[172:179], v[204:211], v[82:85]
	v_mfma_f32_16x16x128_f8f6f4 v[54:57], v[150:157], v[212:219], v[54:57]
	v_mfma_f32_16x16x128_f8f6f4 v[50:53], v[172:179], v[212:219], v[50:53]
	v_mfma_f32_16x16x128_f8f6f4 v[38:41], v[150:157], v[220:227], v[38:41]
	v_mfma_f32_16x16x128_f8f6f4 v[34:37], v[172:179], v[220:227], v[34:37]
	v_mfma_f32_16x16x128_f8f6f4 v[22:25], v[150:157], v[228:235], v[22:25]
	v_mfma_f32_16x16x128_f8f6f4 v[18:21], v[172:179], v[228:235], v[18:21]
	s_setprio 0
	s_setprio 1
	v_mfma_f32_16x16x128_f8f6f4 v[70:73], v[180:187], v[204:211], v[70:73]
	v_mfma_f32_16x16x128_f8f6f4 v[66:69], v[188:195], v[204:211], v[66:69]
	v_mfma_f32_16x16x128_f8f6f4 v[46:49], v[180:187], v[212:219], v[46:49]
	v_mfma_f32_16x16x128_f8f6f4 v[42:45], v[188:195], v[212:219], v[42:45]
	v_mfma_f32_16x16x128_f8f6f4 v[30:33], v[180:187], v[220:227], v[30:33]
	v_mfma_f32_16x16x128_f8f6f4 v[26:29], v[188:195], v[220:227], v[26:29]
	v_mfma_f32_16x16x128_f8f6f4 v[14:17], v[180:187], v[228:235], v[14:17]
	v_mfma_f32_16x16x128_f8f6f4 v[10:13], v[188:195], v[228:235], v[10:13]
	s_setprio 0
	s_barrier
	s_andn2_b64 s[10:11], exec, s[8:9]
	s_andn2_b64 vcc, exec, s[8:9]
	s_cbranch_vccnz .LBB0_3427
	s_add_u32 s8, s46, 0x20080
	s_addc_u32 s9, s47, 0
	s_mov_b32 m0, s63
	v_lshl_add_u64 v[150:151], s[8:9], 0, v[138:139]
	v_lshl_add_u64 v[152:153], s[8:9], 0, v[142:143]
	global_load_lds_dwordx4 v[150:151], off
	s_mov_b32 m0, s69
	s_nop 0
	global_load_lds_dwordx4 v[152:153], off
